# router: interleaved logit reductions and hoisted LDS weight reads; packed accumulator clears in GEMM unit headers
# baseline (speedup 1.0000x reference)
;     __device__ __forceinline__ const char* aptr(const Unit& u) const { return (const char*)(A + (size_t)u.pm * BM * lda); }
;     __device__ __forceinline__ const char* bptr(const Unit& u) const { return (const char*)(Bt + (size_t)u.pn * BM * ldb); }
;     __device__ __forceinline__ const char* aptr(const Unit& u) const { return (const char*)(A + (size_t)u.pm * BM * lda + koff(u)); }
;     __device__ __forceinline__ const char* bptr(const Unit& u) const { return (const char*)(Bt + (size_t)u.pn * BM * ldb + koff(u)); }
;     __device__ __forceinline__ const char* aptr(const Unit& u) const { return (const char*)(A + (size_t)u.pm * BM * lda + koff(u)); }
;     __device__ __forceinline__ const char* bptr(const Unit& u) const { return (const char*)(Bt + (size_t)u.pn * BM * ldb + koff(u)); }
; #define PG8_GOFF(dst, u) do { if constexpr (GA) { _Pragma("unroll") for (int h_ = 0; h_ < 2; ++h_) _Pragma("unroll") for (int i_ = 0; i_ < 2; ++i_) \
;         dst[h_][i_] = (unsigned)(S.grow(u, h_ * HALF + gR[i_]) * S.lda + gC[i_]) * 2u; } } while (0)
;     __device__ __forceinline__ const char* aptr(const Unit& u) const { const int g = u.pm / nM, pm = u.pm % nM; return (const char*)(A + (size_t)g * sA + (size_t)pm * BM * lda); }
; template <class Epi, class Sched>
; __device__ __forceinline__ void gemm_phase(const int WID_, PG8_LAS unsigned char* lds, const Sched& S, const Epi& E) {
;     ...
;         const char* nA = has_next ? S.aptr(nxt) : cA; const char* nB = has_next ? S.bptr(nxt) : cB;
;         if (has_next) PG8_GOFF(vgn, nxt); else { if constexpr (GA) { _Pragma("unroll") for (int h_ = 0; h_ < 2; ++h_) _Pragma("unroll") for (int i_ = 0; i_ < 2; ++i_) vgn[h_][i_] = vgc[h_][i_]; } }
;         for (int t = 0; t < nt; t += 2) {
;             const bool last = (t == nt - 2);
;             const char* a1 = cA + (size_t)(t + 1) * kstep;
;             const char* a2 = last ? nA : cA + (size_t)(t + 2) * kstep; const char* b2 = last ? nB : cB + (size_t)(t + 2) * kstep;
;             const char* a3 = a2 + kstep; const char* b3 = b2 + kstep;
;     ...
; #pragma unroll
;         for (int a = 0; a < 2; ++a)
; #pragma unroll
;             for (int b = 0; b < 2; ++b)
; #pragma unroll
;                 for (int m = 0; m < 4; ++m)
; #pragma unroll
;                     for (int n = 0; n < 2; ++n) acc[a][b][m][n] = (f32x4){0.f, 0.f, 0.f, 0.f};
;         cur = nxt; cA = nA; cB = nB; ++ui;
.LBB0_113:
	s_ashr_i32 s13, s12, 31
	s_lshl_b64 s[14:15], s[12:13], 19
	s_add_u32 s14, s26, s14
	s_addc_u32 s15, s27, s15
	s_and_b64 s[16:17], s[0:1], exec
	s_cselect_b32 s3, s15, s21
	s_cselect_b32 s13, s14, s20
	s_ashr_i32 s11, s10, 31
	s_lshl_b64 s[16:17], s[10:11], 19
	s_add_u32 s16, s52, s16
	s_addc_u32 s17, s53, s17
	s_and_b64 s[28:29], s[0:1], exec
	s_cselect_b32 s11, s17, s23
	s_cselect_b32 s19, s16, s22
	s_add_u32 s20, s20, 0x40080
	s_addc_u32 s21, s21, 0
	s_add_u32 s46, s22, 0x100
	v_mov_b32_e32 v0, 0
	s_addc_u32 s47, s23, 0
	s_mov_b32 s48, -2
	v_mov_b32_e32 v1, v0
	v_pk_mov_b32 v[2:3], v[0:1], v[0:1]
	v_pk_mov_b32 v[4:5], v[0:1], v[0:1]
	v_pk_mov_b32 v[6:7], v[0:1], v[0:1]
	v_pk_mov_b32 v[8:9], v[0:1], v[0:1]
	v_pk_mov_b32 v[10:11], v[0:1], v[0:1]
	v_pk_mov_b32 v[12:13], v[0:1], v[0:1]
	v_pk_mov_b32 v[14:15], v[0:1], v[0:1]
	v_pk_mov_b32 v[16:17], v[0:1], v[0:1]
	v_pk_mov_b32 v[18:19], v[0:1], v[0:1]
	v_pk_mov_b32 v[20:21], v[0:1], v[0:1]
	v_pk_mov_b32 v[22:23], v[0:1], v[0:1]
	v_pk_mov_b32 v[24:25], v[0:1], v[0:1]
	v_pk_mov_b32 v[26:27], v[0:1], v[0:1]
	v_pk_mov_b32 v[28:29], v[0:1], v[0:1]
	v_pk_mov_b32 v[30:31], v[0:1], v[0:1]
	v_pk_mov_b32 v[32:33], v[0:1], v[0:1]
	v_pk_mov_b32 v[34:35], v[0:1], v[0:1]
	v_pk_mov_b32 v[36:37], v[0:1], v[0:1]
	v_pk_mov_b32 v[38:39], v[0:1], v[0:1]
	v_pk_mov_b32 v[40:41], v[0:1], v[0:1]
	v_pk_mov_b32 v[42:43], v[0:1], v[0:1]
	v_pk_mov_b32 v[44:45], v[0:1], v[0:1]
	v_pk_mov_b32 v[46:47], v[0:1], v[0:1]
	v_pk_mov_b32 v[48:49], v[0:1], v[0:1]
	v_pk_mov_b32 v[50:51], v[0:1], v[0:1]
	v_pk_mov_b32 v[52:53], v[0:1], v[0:1]
	v_pk_mov_b32 v[54:55], v[0:1], v[0:1]
	v_pk_mov_b32 v[56:57], v[0:1], v[0:1]
	v_pk_mov_b32 v[58:59], v[0:1], v[0:1]
	v_pk_mov_b32 v[60:61], v[0:1], v[0:1]
	v_pk_mov_b32 v[62:63], v[0:1], v[0:1]
	v_pk_mov_b32 v[64:65], v[0:1], v[0:1]
	v_pk_mov_b32 v[66:67], v[0:1], v[0:1]
	v_pk_mov_b32 v[68:69], v[0:1], v[0:1]
	v_pk_mov_b32 v[70:71], v[0:1], v[0:1]
	v_pk_mov_b32 v[72:73], v[0:1], v[0:1]
	v_pk_mov_b32 v[74:75], v[0:1], v[0:1]
	v_pk_mov_b32 v[76:77], v[0:1], v[0:1]
	v_pk_mov_b32 v[78:79], v[0:1], v[0:1]
	v_pk_mov_b32 v[80:81], v[0:1], v[0:1]
	v_pk_mov_b32 v[82:83], v[0:1], v[0:1]
	v_pk_mov_b32 v[84:85], v[0:1], v[0:1]
	v_pk_mov_b32 v[86:87], v[0:1], v[0:1]
	v_pk_mov_b32 v[88:89], v[0:1], v[0:1]
	v_pk_mov_b32 v[90:91], v[0:1], v[0:1]
	v_pk_mov_b32 v[92:93], v[0:1], v[0:1]
	v_pk_mov_b32 v[94:95], v[0:1], v[0:1]
	v_pk_mov_b32 v[96:97], v[0:1], v[0:1]
	v_pk_mov_b32 v[98:99], v[0:1], v[0:1]
	v_pk_mov_b32 v[100:101], v[0:1], v[0:1]
	v_pk_mov_b32 v[102:103], v[0:1], v[0:1]
	v_pk_mov_b32 v[104:105], v[0:1], v[0:1]
	v_pk_mov_b32 v[106:107], v[0:1], v[0:1]
	v_pk_mov_b32 v[108:109], v[0:1], v[0:1]
	v_pk_mov_b32 v[110:111], v[0:1], v[0:1]
	v_pk_mov_b32 v[112:113], v[0:1], v[0:1]
	v_pk_mov_b32 v[114:115], v[0:1], v[0:1]
	v_pk_mov_b32 v[116:117], v[0:1], v[0:1]
	v_pk_mov_b32 v[118:119], v[0:1], v[0:1]
	v_pk_mov_b32 v[120:121], v[0:1], v[0:1]
	v_pk_mov_b32 v[122:123], v[0:1], v[0:1]
	v_pk_mov_b32 v[124:125], v[0:1], v[0:1]
	v_pk_mov_b32 v[126:127], v[0:1], v[0:1]

;     __device__ __forceinline__ const char* aptr(const Unit& u) const { return (const char*)(A + (size_t)u.pm * BM * lda); }
;     __device__ __forceinline__ const char* bptr(const Unit& u) const { return (const char*)(Bt + (size_t)u.pn * BM * ldb); }
;     __device__ __forceinline__ const char* aptr(const Unit& u) const { return (const char*)(A + (size_t)u.pm * BM * lda + koff(u)); }
;     __device__ __forceinline__ const char* bptr(const Unit& u) const { return (const char*)(Bt + (size_t)u.pn * BM * ldb + koff(u)); }
;     __device__ __forceinline__ const char* aptr(const Unit& u) const { return (const char*)(A + (size_t)u.pm * BM * lda + koff(u)); }
;     __device__ __forceinline__ const char* bptr(const Unit& u) const { return (const char*)(Bt + (size_t)u.pn * BM * ldb + koff(u)); }
; #define PG8_GOFF(dst, u) do { if constexpr (GA) { _Pragma("unroll") for (int h_ = 0; h_ < 2; ++h_) _Pragma("unroll") for (int i_ = 0; i_ < 2; ++i_) \
;         dst[h_][i_] = (unsigned)(S.grow(u, h_ * HALF + gR[i_]) * S.lda + gC[i_]) * 2u; } } while (0)
;     __device__ __forceinline__ const char* aptr(const Unit& u) const { const int g = u.pm / nM, pm = u.pm % nM; return (const char*)(A + (size_t)g * sA + (size_t)pm * BM * lda); }
; template <class Epi, class Sched>
; __device__ __forceinline__ void gemm_phase(const int WID_, PG8_LAS unsigned char* lds, const Sched& S, const Epi& E) {
;     ...
;         const char* nA = has_next ? S.aptr(nxt) : cA; const char* nB = has_next ? S.bptr(nxt) : cB;
;         if (has_next) PG8_GOFF(vgn, nxt); else { if constexpr (GA) { _Pragma("unroll") for (int h_ = 0; h_ < 2; ++h_) _Pragma("unroll") for (int i_ = 0; i_ < 2; ++i_) vgn[h_][i_] = vgc[h_][i_]; } }
;         for (int t = 0; t < nt; t += 2) {
;             const bool last = (t == nt - 2);
;             const char* a1 = cA + (size_t)(t + 1) * kstep;
;             const char* a2 = last ? nA : cA + (size_t)(t + 2) * kstep; const char* b2 = last ? nB : cB + (size_t)(t + 2) * kstep;
;             const char* a3 = a2 + kstep; const char* b3 = b2 + kstep;
;     ...
; #pragma unroll
;         for (int a = 0; a < 2; ++a)
; #pragma unroll
;             for (int b = 0; b < 2; ++b)
; #pragma unroll
;                 for (int m = 0; m < 4; ++m)
; #pragma unroll
;                     for (int n = 0; n < 2; ++n) acc[a][b][m][n] = (f32x4){0.f, 0.f, 0.f, 0.f};
;         cur = nxt; cA = nA; cB = nB; ++ui;
.LBB0_262:
	s_add_u32 s6, s6, 0x20080
	s_addc_u32 s7, s7, 0
	s_add_u32 s5, s8, 0x100
	v_mov_b32_e32 v0, 0
	s_addc_u32 s21, s9, 0
	s_mov_b32 s35, -2
	v_mov_b32_e32 v1, v0
	v_pk_mov_b32 v[2:3], v[0:1], v[0:1]
	v_pk_mov_b32 v[4:5], v[0:1], v[0:1]
	v_pk_mov_b32 v[6:7], v[0:1], v[0:1]
	v_pk_mov_b32 v[8:9], v[0:1], v[0:1]
	v_pk_mov_b32 v[10:11], v[0:1], v[0:1]
	v_pk_mov_b32 v[12:13], v[0:1], v[0:1]
	v_pk_mov_b32 v[14:15], v[0:1], v[0:1]
	v_pk_mov_b32 v[16:17], v[0:1], v[0:1]
	v_pk_mov_b32 v[18:19], v[0:1], v[0:1]
	v_pk_mov_b32 v[20:21], v[0:1], v[0:1]
	v_pk_mov_b32 v[22:23], v[0:1], v[0:1]
	v_pk_mov_b32 v[24:25], v[0:1], v[0:1]
	v_pk_mov_b32 v[26:27], v[0:1], v[0:1]
	v_pk_mov_b32 v[28:29], v[0:1], v[0:1]
	v_pk_mov_b32 v[30:31], v[0:1], v[0:1]
	v_pk_mov_b32 v[32:33], v[0:1], v[0:1]
	v_pk_mov_b32 v[34:35], v[0:1], v[0:1]
	v_pk_mov_b32 v[36:37], v[0:1], v[0:1]
	v_pk_mov_b32 v[38:39], v[0:1], v[0:1]
	v_pk_mov_b32 v[40:41], v[0:1], v[0:1]
	v_pk_mov_b32 v[42:43], v[0:1], v[0:1]
	v_pk_mov_b32 v[44:45], v[0:1], v[0:1]
	v_pk_mov_b32 v[46:47], v[0:1], v[0:1]
	v_pk_mov_b32 v[48:49], v[0:1], v[0:1]
	v_pk_mov_b32 v[50:51], v[0:1], v[0:1]
	v_pk_mov_b32 v[52:53], v[0:1], v[0:1]
	v_pk_mov_b32 v[54:55], v[0:1], v[0:1]
	v_pk_mov_b32 v[56:57], v[0:1], v[0:1]
	v_pk_mov_b32 v[58:59], v[0:1], v[0:1]
	v_pk_mov_b32 v[60:61], v[0:1], v[0:1]
	v_pk_mov_b32 v[62:63], v[0:1], v[0:1]
	v_pk_mov_b32 v[64:65], v[0:1], v[0:1]
	v_pk_mov_b32 v[66:67], v[0:1], v[0:1]
	v_pk_mov_b32 v[68:69], v[0:1], v[0:1]
	v_pk_mov_b32 v[70:71], v[0:1], v[0:1]
	v_pk_mov_b32 v[72:73], v[0:1], v[0:1]
	v_pk_mov_b32 v[74:75], v[0:1], v[0:1]
	v_pk_mov_b32 v[76:77], v[0:1], v[0:1]
	v_pk_mov_b32 v[78:79], v[0:1], v[0:1]
	v_pk_mov_b32 v[80:81], v[0:1], v[0:1]
	v_pk_mov_b32 v[82:83], v[0:1], v[0:1]
	v_pk_mov_b32 v[84:85], v[0:1], v[0:1]
	v_pk_mov_b32 v[86:87], v[0:1], v[0:1]
	v_pk_mov_b32 v[88:89], v[0:1], v[0:1]
	v_pk_mov_b32 v[90:91], v[0:1], v[0:1]
	v_pk_mov_b32 v[92:93], v[0:1], v[0:1]
	v_pk_mov_b32 v[94:95], v[0:1], v[0:1]
	v_pk_mov_b32 v[96:97], v[0:1], v[0:1]
	v_pk_mov_b32 v[98:99], v[0:1], v[0:1]
	v_pk_mov_b32 v[100:101], v[0:1], v[0:1]
	v_pk_mov_b32 v[102:103], v[0:1], v[0:1]
	v_pk_mov_b32 v[104:105], v[0:1], v[0:1]
	v_pk_mov_b32 v[106:107], v[0:1], v[0:1]
	v_pk_mov_b32 v[108:109], v[0:1], v[0:1]
	v_pk_mov_b32 v[110:111], v[0:1], v[0:1]
	v_pk_mov_b32 v[112:113], v[0:1], v[0:1]
	v_pk_mov_b32 v[114:115], v[0:1], v[0:1]
	v_pk_mov_b32 v[116:117], v[0:1], v[0:1]
	v_pk_mov_b32 v[118:119], v[0:1], v[0:1]
	v_pk_mov_b32 v[120:121], v[0:1], v[0:1]
	v_pk_mov_b32 v[122:123], v[0:1], v[0:1]
	v_pk_mov_b32 v[124:125], v[0:1], v[0:1]
	v_pk_mov_b32 v[126:127], v[0:1], v[0:1]

;     __device__ __forceinline__ const char* aptr(const Unit& u) const { return (const char*)(A + (size_t)u.pm * BM * lda); }
;     __device__ __forceinline__ const char* bptr(const Unit& u) const { return (const char*)(Bt + (size_t)u.pn * BM * ldb); }
;     __device__ __forceinline__ const char* aptr(const Unit& u) const { return (const char*)(A + (size_t)u.pm * BM * lda + koff(u)); }
;     __device__ __forceinline__ const char* bptr(const Unit& u) const { return (const char*)(Bt + (size_t)u.pn * BM * ldb + koff(u)); }
;     __device__ __forceinline__ const char* aptr(const Unit& u) const { return (const char*)(A + (size_t)u.pm * BM * lda + koff(u)); }
;     __device__ __forceinline__ const char* bptr(const Unit& u) const { return (const char*)(Bt + (size_t)u.pn * BM * ldb + koff(u)); }
; #define PG8_GOFF(dst, u) do { if constexpr (GA) { _Pragma("unroll") for (int h_ = 0; h_ < 2; ++h_) _Pragma("unroll") for (int i_ = 0; i_ < 2; ++i_) \
;         dst[h_][i_] = (unsigned)(S.grow(u, h_ * HALF + gR[i_]) * S.lda + gC[i_]) * 2u; } } while (0)
;     __device__ __forceinline__ const char* aptr(const Unit& u) const { const int g = u.pm / nM, pm = u.pm % nM; return (const char*)(A + (size_t)g * sA + (size_t)pm * BM * lda); }
; template <class Epi, class Sched>
; __device__ __forceinline__ void gemm_phase(const int WID_, PG8_LAS unsigned char* lds, const Sched& S, const Epi& E) {
;     ...
;         const char* nA = has_next ? S.aptr(nxt) : cA; const char* nB = has_next ? S.bptr(nxt) : cB;
;         if (has_next) PG8_GOFF(vgn, nxt); else { if constexpr (GA) { _Pragma("unroll") for (int h_ = 0; h_ < 2; ++h_) _Pragma("unroll") for (int i_ = 0; i_ < 2; ++i_) vgn[h_][i_] = vgc[h_][i_]; } }
;         for (int t = 0; t < nt; t += 2) {
;             const bool last = (t == nt - 2);
;             const char* a1 = cA + (size_t)(t + 1) * kstep;
;             const char* a2 = last ? nA : cA + (size_t)(t + 2) * kstep; const char* b2 = last ? nB : cB + (size_t)(t + 2) * kstep;
;             const char* a3 = a2 + kstep; const char* b3 = b2 + kstep;
;     ...
; #pragma unroll
;         for (int a = 0; a < 2; ++a)
; #pragma unroll
;             for (int b = 0; b < 2; ++b)
; #pragma unroll
;                 for (int m = 0; m < 4; ++m)
; #pragma unroll
;                     for (int n = 0; n < 2; ++n) acc[a][b][m][n] = (f32x4){0.f, 0.f, 0.f, 0.f};
;         cur = nxt; cA = nA; cB = nB; ++ui;
.LBB0_1562:
	s_ashr_i32 s37, s36, 31
	s_lshl_b64 s[40:41], s[36:37], 19
	s_add_u32 s40, s34, s40
	s_addc_u32 s41, s35, s41
	s_and_b64 s[44:45], s[42:43], exec
	s_cselect_b32 s37, s41, s47
	s_cselect_b32 s67, s40, s46
	s_ashr_i32 s39, s38, 31
	s_lshl_b64 s[44:45], s[38:39], 19
	v_readlane_b32 s50, v243, 49
	v_readlane_b32 s51, v243, 50
	s_add_u32 s44, s50, s44
	s_addc_u32 s45, s51, s45
	s_and_b64 s[50:51], s[42:43], exec
	s_cselect_b32 s39, s45, s49
	s_cselect_b32 s68, s44, s48
	s_add_u32 s46, s46, 0x40080
	s_addc_u32 s47, s47, 0
	s_add_u32 s69, s48, 0x100
	v_mov_b32_e32 v0, 0
	s_addc_u32 s70, s49, 0
	s_mov_b32 s71, -2
	v_mov_b32_e32 v1, v0
	v_pk_mov_b32 v[2:3], v[0:1], v[0:1]
	v_pk_mov_b32 v[4:5], v[0:1], v[0:1]
	v_pk_mov_b32 v[6:7], v[0:1], v[0:1]
	v_pk_mov_b32 v[8:9], v[0:1], v[0:1]
	v_pk_mov_b32 v[10:11], v[0:1], v[0:1]
	v_pk_mov_b32 v[12:13], v[0:1], v[0:1]
	v_pk_mov_b32 v[14:15], v[0:1], v[0:1]
	v_pk_mov_b32 v[16:17], v[0:1], v[0:1]
	v_pk_mov_b32 v[18:19], v[0:1], v[0:1]
	v_pk_mov_b32 v[20:21], v[0:1], v[0:1]
	v_pk_mov_b32 v[22:23], v[0:1], v[0:1]
	v_pk_mov_b32 v[24:25], v[0:1], v[0:1]
	v_pk_mov_b32 v[26:27], v[0:1], v[0:1]
	v_pk_mov_b32 v[28:29], v[0:1], v[0:1]
	v_pk_mov_b32 v[30:31], v[0:1], v[0:1]
	v_pk_mov_b32 v[32:33], v[0:1], v[0:1]
	v_pk_mov_b32 v[34:35], v[0:1], v[0:1]
	v_pk_mov_b32 v[36:37], v[0:1], v[0:1]
	v_pk_mov_b32 v[38:39], v[0:1], v[0:1]
	v_pk_mov_b32 v[40:41], v[0:1], v[0:1]
	v_pk_mov_b32 v[42:43], v[0:1], v[0:1]
	v_pk_mov_b32 v[44:45], v[0:1], v[0:1]
	v_pk_mov_b32 v[46:47], v[0:1], v[0:1]
	v_pk_mov_b32 v[48:49], v[0:1], v[0:1]
	v_pk_mov_b32 v[50:51], v[0:1], v[0:1]
	v_pk_mov_b32 v[52:53], v[0:1], v[0:1]
	v_pk_mov_b32 v[54:55], v[0:1], v[0:1]
	v_pk_mov_b32 v[56:57], v[0:1], v[0:1]
	v_pk_mov_b32 v[58:59], v[0:1], v[0:1]
	v_pk_mov_b32 v[60:61], v[0:1], v[0:1]
	v_pk_mov_b32 v[62:63], v[0:1], v[0:1]
	v_pk_mov_b32 v[64:65], v[0:1], v[0:1]
	v_pk_mov_b32 v[66:67], v[0:1], v[0:1]
	v_pk_mov_b32 v[68:69], v[0:1], v[0:1]
	v_pk_mov_b32 v[70:71], v[0:1], v[0:1]
	v_pk_mov_b32 v[72:73], v[0:1], v[0:1]
	v_pk_mov_b32 v[74:75], v[0:1], v[0:1]
	v_pk_mov_b32 v[76:77], v[0:1], v[0:1]
	v_pk_mov_b32 v[78:79], v[0:1], v[0:1]
	v_pk_mov_b32 v[80:81], v[0:1], v[0:1]
	v_pk_mov_b32 v[82:83], v[0:1], v[0:1]
	v_pk_mov_b32 v[84:85], v[0:1], v[0:1]
	v_pk_mov_b32 v[86:87], v[0:1], v[0:1]
	v_pk_mov_b32 v[88:89], v[0:1], v[0:1]
	v_pk_mov_b32 v[90:91], v[0:1], v[0:1]
	v_pk_mov_b32 v[92:93], v[0:1], v[0:1]
	v_pk_mov_b32 v[94:95], v[0:1], v[0:1]
	v_pk_mov_b32 v[96:97], v[0:1], v[0:1]
	v_pk_mov_b32 v[98:99], v[0:1], v[0:1]
	v_pk_mov_b32 v[100:101], v[0:1], v[0:1]
	v_pk_mov_b32 v[102:103], v[0:1], v[0:1]
	v_pk_mov_b32 v[104:105], v[0:1], v[0:1]
	v_pk_mov_b32 v[106:107], v[0:1], v[0:1]
	v_pk_mov_b32 v[108:109], v[0:1], v[0:1]
	v_pk_mov_b32 v[110:111], v[0:1], v[0:1]
	v_pk_mov_b32 v[112:113], v[0:1], v[0:1]
	v_pk_mov_b32 v[114:115], v[0:1], v[0:1]
	v_pk_mov_b32 v[116:117], v[0:1], v[0:1]
	v_pk_mov_b32 v[118:119], v[0:1], v[0:1]
	v_pk_mov_b32 v[120:121], v[0:1], v[0:1]
	v_pk_mov_b32 v[122:123], v[0:1], v[0:1]
	v_pk_mov_b32 v[124:125], v[0:1], v[0:1]
	v_pk_mov_b32 v[126:127], v[0:1], v[0:1]

;     __device__ __forceinline__ const char* aptr(const Unit& u) const { return (const char*)(A + (size_t)u.pm * BM * lda); }
;     __device__ __forceinline__ const char* bptr(const Unit& u) const { return (const char*)(Bt + (size_t)u.pn * BM * ldb); }
;     __device__ __forceinline__ const char* aptr(const Unit& u) const { return (const char*)(A + (size_t)u.pm * BM * lda + koff(u)); }
;     __device__ __forceinline__ const char* bptr(const Unit& u) const { return (const char*)(Bt + (size_t)u.pn * BM * ldb + koff(u)); }
;     __device__ __forceinline__ const char* aptr(const Unit& u) const { return (const char*)(A + (size_t)u.pm * BM * lda + koff(u)); }
;     __device__ __forceinline__ const char* bptr(const Unit& u) const { return (const char*)(Bt + (size_t)u.pn * BM * ldb + koff(u)); }
; #define PG8_GOFF(dst, u) do { if constexpr (GA) { _Pragma("unroll") for (int h_ = 0; h_ < 2; ++h_) _Pragma("unroll") for (int i_ = 0; i_ < 2; ++i_) \
;         dst[h_][i_] = (unsigned)(S.grow(u, h_ * HALF + gR[i_]) * S.lda + gC[i_]) * 2u; } } while (0)
;     __device__ __forceinline__ const char* aptr(const Unit& u) const { const int g = u.pm / nM, pm = u.pm % nM; return (const char*)(A + (size_t)g * sA + (size_t)pm * BM * lda); }
; template <class Epi, class Sched>
; __device__ __forceinline__ void gemm_phase(const int WID_, PG8_LAS unsigned char* lds, const Sched& S, const Epi& E) {
;     ...
;         const char* nA = has_next ? S.aptr(nxt) : cA; const char* nB = has_next ? S.bptr(nxt) : cB;
;         if (has_next) PG8_GOFF(vgn, nxt); else { if constexpr (GA) { _Pragma("unroll") for (int h_ = 0; h_ < 2; ++h_) _Pragma("unroll") for (int i_ = 0; i_ < 2; ++i_) vgn[h_][i_] = vgc[h_][i_]; } }
;         for (int t = 0; t < nt; t += 2) {
;             const bool last = (t == nt - 2);
;             const char* a1 = cA + (size_t)(t + 1) * kstep;
;             const char* a2 = last ? nA : cA + (size_t)(t + 2) * kstep; const char* b2 = last ? nB : cB + (size_t)(t + 2) * kstep;
;             const char* a3 = a2 + kstep; const char* b3 = b2 + kstep;
;     ...
; #pragma unroll
;         for (int a = 0; a < 2; ++a)
; #pragma unroll
;             for (int b = 0; b < 2; ++b)
; #pragma unroll
;                 for (int m = 0; m < 4; ++m)
; #pragma unroll
;                     for (int n = 0; n < 2; ++n) acc[a][b][m][n] = (f32x4){0.f, 0.f, 0.f, 0.f};
;         cur = nxt; cA = nA; cB = nB; ++ui;
.LBB0_1582:
	s_ashr_i32 s37, s36, 31
	s_lshl_b64 s[40:41], s[36:37], 19
	s_add_u32 s40, s34, s40
	s_addc_u32 s41, s35, s41
	s_and_b64 s[44:45], s[42:43], exec
	s_cselect_b32 s37, s41, s47
	s_cselect_b32 s67, s40, s46
	s_ashr_i32 s39, s38, 31
	s_lshl_b64 s[44:45], s[38:39], 19
	v_readlane_b32 s50, v243, 51
	v_readlane_b32 s51, v243, 52
	s_add_u32 s44, s50, s44
	s_addc_u32 s45, s51, s45
	s_and_b64 s[50:51], s[42:43], exec
	s_cselect_b32 s39, s45, s49
	s_cselect_b32 s68, s44, s48
	s_add_u32 s46, s46, 0x40080
	s_addc_u32 s47, s47, 0
	s_add_u32 s69, s48, 0x100
	v_mov_b32_e32 v0, 0
	s_addc_u32 s70, s49, 0
	s_mov_b32 s71, -2
	v_mov_b32_e32 v1, v0
	v_pk_mov_b32 v[2:3], v[0:1], v[0:1]
	v_pk_mov_b32 v[4:5], v[0:1], v[0:1]
	v_pk_mov_b32 v[6:7], v[0:1], v[0:1]
	v_pk_mov_b32 v[8:9], v[0:1], v[0:1]
	v_pk_mov_b32 v[10:11], v[0:1], v[0:1]
	v_pk_mov_b32 v[12:13], v[0:1], v[0:1]
	v_pk_mov_b32 v[14:15], v[0:1], v[0:1]
	v_pk_mov_b32 v[16:17], v[0:1], v[0:1]
	v_pk_mov_b32 v[18:19], v[0:1], v[0:1]
	v_pk_mov_b32 v[20:21], v[0:1], v[0:1]
	v_pk_mov_b32 v[22:23], v[0:1], v[0:1]
	v_pk_mov_b32 v[24:25], v[0:1], v[0:1]
	v_pk_mov_b32 v[26:27], v[0:1], v[0:1]
	v_pk_mov_b32 v[28:29], v[0:1], v[0:1]
	v_pk_mov_b32 v[30:31], v[0:1], v[0:1]
	v_pk_mov_b32 v[32:33], v[0:1], v[0:1]
	v_pk_mov_b32 v[34:35], v[0:1], v[0:1]
	v_pk_mov_b32 v[36:37], v[0:1], v[0:1]
	v_pk_mov_b32 v[38:39], v[0:1], v[0:1]
	v_pk_mov_b32 v[40:41], v[0:1], v[0:1]
	v_pk_mov_b32 v[42:43], v[0:1], v[0:1]
	v_pk_mov_b32 v[44:45], v[0:1], v[0:1]
	v_pk_mov_b32 v[46:47], v[0:1], v[0:1]
	v_pk_mov_b32 v[48:49], v[0:1], v[0:1]
	v_pk_mov_b32 v[50:51], v[0:1], v[0:1]
	v_pk_mov_b32 v[52:53], v[0:1], v[0:1]
	v_pk_mov_b32 v[54:55], v[0:1], v[0:1]
	v_pk_mov_b32 v[56:57], v[0:1], v[0:1]
	v_pk_mov_b32 v[58:59], v[0:1], v[0:1]
	v_pk_mov_b32 v[60:61], v[0:1], v[0:1]
	v_pk_mov_b32 v[62:63], v[0:1], v[0:1]
	v_pk_mov_b32 v[64:65], v[0:1], v[0:1]
	v_pk_mov_b32 v[66:67], v[0:1], v[0:1]
	v_pk_mov_b32 v[68:69], v[0:1], v[0:1]
	v_pk_mov_b32 v[70:71], v[0:1], v[0:1]
	v_pk_mov_b32 v[72:73], v[0:1], v[0:1]
	v_pk_mov_b32 v[74:75], v[0:1], v[0:1]
	v_pk_mov_b32 v[76:77], v[0:1], v[0:1]
	v_pk_mov_b32 v[78:79], v[0:1], v[0:1]
	v_pk_mov_b32 v[80:81], v[0:1], v[0:1]
	v_pk_mov_b32 v[82:83], v[0:1], v[0:1]
	v_pk_mov_b32 v[84:85], v[0:1], v[0:1]
	v_pk_mov_b32 v[86:87], v[0:1], v[0:1]
	v_pk_mov_b32 v[88:89], v[0:1], v[0:1]
	v_pk_mov_b32 v[90:91], v[0:1], v[0:1]
	v_pk_mov_b32 v[92:93], v[0:1], v[0:1]
	v_pk_mov_b32 v[94:95], v[0:1], v[0:1]
	v_pk_mov_b32 v[96:97], v[0:1], v[0:1]
	v_pk_mov_b32 v[98:99], v[0:1], v[0:1]
	v_pk_mov_b32 v[100:101], v[0:1], v[0:1]
	v_pk_mov_b32 v[102:103], v[0:1], v[0:1]
	v_pk_mov_b32 v[104:105], v[0:1], v[0:1]
	v_pk_mov_b32 v[106:107], v[0:1], v[0:1]
	v_pk_mov_b32 v[108:109], v[0:1], v[0:1]
	v_pk_mov_b32 v[110:111], v[0:1], v[0:1]
	v_pk_mov_b32 v[112:113], v[0:1], v[0:1]
	v_pk_mov_b32 v[114:115], v[0:1], v[0:1]
	v_pk_mov_b32 v[116:117], v[0:1], v[0:1]
	v_pk_mov_b32 v[118:119], v[0:1], v[0:1]
	v_pk_mov_b32 v[120:121], v[0:1], v[0:1]
	v_pk_mov_b32 v[122:123], v[0:1], v[0:1]
	v_pk_mov_b32 v[124:125], v[0:1], v[0:1]
	v_pk_mov_b32 v[126:127], v[0:1], v[0:1]

; #define PG8_WAIT_V(n) asm volatile("s_waitcnt vmcnt(" #n ")" ::: "memory")
; template <class Epi, class Sched>
; __device__ __forceinline__ void gemm_phase(const int WID_, PG8_LAS unsigned char* lds, const Sched& S, const Epi& E) {
;     ...
;         const bool has_next = S.next(ui + 1, nxt);
;         const char* nA = has_next ? S.aptr(nxt) : cA; const char* nB = has_next ? S.bptr(nxt) : cB;
;         if (has_next) PG8_GOFF(vgn, nxt); else { if constexpr (GA) { _Pragma("unroll") for (int h_ = 0; h_ < 2; ++h_) _Pragma("unroll") for (int i_ = 0; i_ < 2; ++i_) vgn[h_][i_] = vgc[h_][i_]; } }
;         for (int t = 0; t < nt; t += 2) {
;             const bool last = (t == nt - 2);
;             const char* a1 = cA + (size_t)(t + 1) * kstep;
;             const char* a2 = last ? nA : cA + (size_t)(t + 2) * kstep; const char* b2 = last ? nB : cB + (size_t)(t + 2) * kstep;
;             const char* a3 = a2 + kstep; const char* b3 = b2 + kstep;
;             PG8_LDB(B0, 0, 0); PG8_LDB(B1, 0, 1); PG8_SCHED; PG8_LDA(At, 0, 0); PG8_STAGE_A(PG8_SA(1, 1), a1 + hstepA, 1, false);
;             PG8_WAIT_V(8); PG8_WAIT_L(0); PG8_BAR; PG8_MMA(0, 0, At, B0); PG8_MMA(0, 1, At, B1); PG8_BAR; PG8_SCHED;
;             PG8_LDA(At, 0, 1); PG8_STAGE(PG8_SB(0, 0), b2, voffB); PG8_STAGE(PG8_SB(0, 1), b2 + hstepB, voffB); PG8_STAGE_A(PG8_SA(0, 0), a2, 0, last);
;             PG8_WAIT_V(8); PG8_WAIT_L(0); PG8_BAR; PG8_MMA(1, 0, At, B0); PG8_MMA(1, 1, At, B1); PG8_BAR; PG8_SCHED;
;             PG8_LDB(B0, 1, 0); PG8_LDB(B1, 1, 1); PG8_SCHED; PG8_LDA(At, 1, 0); PG8_STAGE_A(PG8_SA(0, 1), a2 + hstepA, 1, last);
;             PG8_WAIT_V(8); PG8_WAIT_L(0); PG8_BAR; PG8_MMA(0, 0, At, B0); PG8_MMA(0, 1, At, B1); PG8_BAR; PG8_SCHED;
;             PG8_LDA(At, 1, 1); PG8_STAGE(PG8_SB(1, 0), b3, voffB); PG8_STAGE(PG8_SB(1, 1), b3 + hstepB, voffB); PG8_STAGE_A(PG8_SA(1, 0), a3, 0, last);
;             PG8_WAIT_V(8); PG8_WAIT_L(0); PG8_BAR; PG8_MMA(1, 0, At, B0); PG8_MMA(1, 1, At, B1); PG8_BAR; PG8_SCHED;
;         }
;         if (wr == 0) PG8_BAR;
;         E(acc, cur, wr, wc, fr, fq);
;         if (!has_next) break;
; #pragma unroll
;         for (int a = 0; a < 2; ++a)
; #pragma unroll
;             for (int b = 0; b < 2; ++b)
; #pragma unroll
;                 for (int m = 0; m < 4; ++m)
; #pragma unroll
;                     for (int n = 0; n < 2; ++n) acc[a][b][m][n] = (f32x4){0.f, 0.f, 0.f, 0.f};
.LBB0_1785:
	s_ashr_i32 s37, s36, 31
	s_lshl_b64 s[38:39], s[36:37], 19
	s_add_u32 s38, s34, s38
	s_addc_u32 s39, s35, s39
	s_and_b64 s[40:41], s[18:19], exec
	s_cselect_b32 s37, s39, s43
	s_cselect_b32 s61, s38, s42
	s_ashr_i32 s23, s22, 31
	s_lshl_b64 s[40:41], s[22:23], 19
	v_readlane_b32 s46, v243, 49
	v_readlane_b32 s47, v243, 50
	s_add_u32 s40, s46, s40
	s_addc_u32 s41, s47, s41
	s_and_b64 s[46:47], s[18:19], exec
	s_cselect_b32 s23, s41, s45
	s_cselect_b32 s62, s40, s44
	s_add_u32 s42, s42, 0x40080
	s_addc_u32 s43, s43, 0
	s_add_u32 s63, s44, 0x100
	v_mov_b32_e32 v0, 0
	s_addc_u32 s66, s45, 0
	s_mov_b32 s67, -2
	v_mov_b32_e32 v1, v0
	v_pk_mov_b32 v[2:3], v[0:1], v[0:1]
	v_pk_mov_b32 v[4:5], v[0:1], v[0:1]
	v_pk_mov_b32 v[6:7], v[0:1], v[0:1]
	v_pk_mov_b32 v[8:9], v[0:1], v[0:1]
	v_pk_mov_b32 v[10:11], v[0:1], v[0:1]
	v_pk_mov_b32 v[12:13], v[0:1], v[0:1]
	v_pk_mov_b32 v[14:15], v[0:1], v[0:1]
	v_pk_mov_b32 v[16:17], v[0:1], v[0:1]
	v_pk_mov_b32 v[18:19], v[0:1], v[0:1]
	v_pk_mov_b32 v[20:21], v[0:1], v[0:1]
	v_pk_mov_b32 v[22:23], v[0:1], v[0:1]
	v_pk_mov_b32 v[24:25], v[0:1], v[0:1]
	v_pk_mov_b32 v[26:27], v[0:1], v[0:1]
	v_pk_mov_b32 v[28:29], v[0:1], v[0:1]
	v_pk_mov_b32 v[30:31], v[0:1], v[0:1]
	v_pk_mov_b32 v[32:33], v[0:1], v[0:1]
	v_pk_mov_b32 v[34:35], v[0:1], v[0:1]
	v_pk_mov_b32 v[36:37], v[0:1], v[0:1]
	v_pk_mov_b32 v[38:39], v[0:1], v[0:1]
	v_pk_mov_b32 v[40:41], v[0:1], v[0:1]
	v_pk_mov_b32 v[42:43], v[0:1], v[0:1]
	v_pk_mov_b32 v[44:45], v[0:1], v[0:1]
	v_pk_mov_b32 v[46:47], v[0:1], v[0:1]
	v_pk_mov_b32 v[48:49], v[0:1], v[0:1]
	v_pk_mov_b32 v[50:51], v[0:1], v[0:1]
	v_pk_mov_b32 v[52:53], v[0:1], v[0:1]
	v_pk_mov_b32 v[54:55], v[0:1], v[0:1]
	v_pk_mov_b32 v[56:57], v[0:1], v[0:1]
	v_pk_mov_b32 v[58:59], v[0:1], v[0:1]
	v_pk_mov_b32 v[60:61], v[0:1], v[0:1]
	v_pk_mov_b32 v[62:63], v[0:1], v[0:1]
	v_pk_mov_b32 v[64:65], v[0:1], v[0:1]
	v_pk_mov_b32 v[66:67], v[0:1], v[0:1]
	v_pk_mov_b32 v[68:69], v[0:1], v[0:1]
	v_pk_mov_b32 v[70:71], v[0:1], v[0:1]
	v_pk_mov_b32 v[72:73], v[0:1], v[0:1]
	v_pk_mov_b32 v[74:75], v[0:1], v[0:1]
	v_pk_mov_b32 v[76:77], v[0:1], v[0:1]
	v_pk_mov_b32 v[78:79], v[0:1], v[0:1]
	v_pk_mov_b32 v[80:81], v[0:1], v[0:1]
	v_pk_mov_b32 v[82:83], v[0:1], v[0:1]
	v_pk_mov_b32 v[84:85], v[0:1], v[0:1]
	v_pk_mov_b32 v[86:87], v[0:1], v[0:1]
	v_pk_mov_b32 v[88:89], v[0:1], v[0:1]
	v_pk_mov_b32 v[90:91], v[0:1], v[0:1]
	v_pk_mov_b32 v[92:93], v[0:1], v[0:1]
	v_pk_mov_b32 v[94:95], v[0:1], v[0:1]
	v_pk_mov_b32 v[96:97], v[0:1], v[0:1]
	v_pk_mov_b32 v[98:99], v[0:1], v[0:1]
	v_pk_mov_b32 v[100:101], v[0:1], v[0:1]
	v_pk_mov_b32 v[102:103], v[0:1], v[0:1]
	v_pk_mov_b32 v[104:105], v[0:1], v[0:1]
	v_pk_mov_b32 v[106:107], v[0:1], v[0:1]
	v_pk_mov_b32 v[108:109], v[0:1], v[0:1]
	v_pk_mov_b32 v[110:111], v[0:1], v[0:1]
	v_pk_mov_b32 v[112:113], v[0:1], v[0:1]
	v_pk_mov_b32 v[114:115], v[0:1], v[0:1]
	v_pk_mov_b32 v[116:117], v[0:1], v[0:1]
	v_pk_mov_b32 v[118:119], v[0:1], v[0:1]
	v_pk_mov_b32 v[120:121], v[0:1], v[0:1]
	v_pk_mov_b32 v[122:123], v[0:1], v[0:1]
	v_pk_mov_b32 v[124:125], v[0:1], v[0:1]
	v_pk_mov_b32 v[126:127], v[0:1], v[0:1]

; #define PG8_WAIT_V(n) asm volatile("s_waitcnt vmcnt(" #n ")" ::: "memory")
; template <class Epi, class Sched>
; __device__ __forceinline__ void gemm_phase(const int WID_, PG8_LAS unsigned char* lds, const Sched& S, const Epi& E) {
;     ...
;         const bool has_next = S.next(ui + 1, nxt);
;         const char* nA = has_next ? S.aptr(nxt) : cA; const char* nB = has_next ? S.bptr(nxt) : cB;
;         if (has_next) PG8_GOFF(vgn, nxt); else { if constexpr (GA) { _Pragma("unroll") for (int h_ = 0; h_ < 2; ++h_) _Pragma("unroll") for (int i_ = 0; i_ < 2; ++i_) vgn[h_][i_] = vgc[h_][i_]; } }
;         for (int t = 0; t < nt; t += 2) {
;             const bool last = (t == nt - 2);
;             const char* a1 = cA + (size_t)(t + 1) * kstep;
;             const char* a2 = last ? nA : cA + (size_t)(t + 2) * kstep; const char* b2 = last ? nB : cB + (size_t)(t + 2) * kstep;
;             const char* a3 = a2 + kstep; const char* b3 = b2 + kstep;
;             PG8_LDB(B0, 0, 0); PG8_LDB(B1, 0, 1); PG8_SCHED; PG8_LDA(At, 0, 0); PG8_STAGE_A(PG8_SA(1, 1), a1 + hstepA, 1, false);
;             PG8_WAIT_V(8); PG8_WAIT_L(0); PG8_BAR; PG8_MMA(0, 0, At, B0); PG8_MMA(0, 1, At, B1); PG8_BAR; PG8_SCHED;
;             PG8_LDA(At, 0, 1); PG8_STAGE(PG8_SB(0, 0), b2, voffB); PG8_STAGE(PG8_SB(0, 1), b2 + hstepB, voffB); PG8_STAGE_A(PG8_SA(0, 0), a2, 0, last);
;             PG8_WAIT_V(8); PG8_WAIT_L(0); PG8_BAR; PG8_MMA(1, 0, At, B0); PG8_MMA(1, 1, At, B1); PG8_BAR; PG8_SCHED;
;             PG8_LDB(B0, 1, 0); PG8_LDB(B1, 1, 1); PG8_SCHED; PG8_LDA(At, 1, 0); PG8_STAGE_A(PG8_SA(0, 1), a2 + hstepA, 1, last);
;             PG8_WAIT_V(8); PG8_WAIT_L(0); PG8_BAR; PG8_MMA(0, 0, At, B0); PG8_MMA(0, 1, At, B1); PG8_BAR; PG8_SCHED;
;             PG8_LDA(At, 1, 1); PG8_STAGE(PG8_SB(1, 0), b3, voffB); PG8_STAGE(PG8_SB(1, 1), b3 + hstepB, voffB); PG8_STAGE_A(PG8_SA(1, 0), a3, 0, last);
;             PG8_WAIT_V(8); PG8_WAIT_L(0); PG8_BAR; PG8_MMA(1, 0, At, B0); PG8_MMA(1, 1, At, B1); PG8_BAR; PG8_SCHED;
;         }
;         if (wr == 0) PG8_BAR;
;         E(acc, cur, wr, wc, fr, fq);
;         if (!has_next) break;
; #pragma unroll
;         for (int a = 0; a < 2; ++a)
; #pragma unroll
;             for (int b = 0; b < 2; ++b)
; #pragma unroll
;                 for (int m = 0; m < 4; ++m)
; #pragma unroll
;                     for (int n = 0; n < 2; ++n) acc[a][b][m][n] = (f32x4){0.f, 0.f, 0.f, 0.f};
.LBB0_1809:
	s_ashr_i32 s37, s36, 31
	s_lshl_b64 s[38:39], s[36:37], 19
	s_add_u32 s38, s34, s38
	s_addc_u32 s39, s35, s39
	s_and_b64 s[40:41], s[18:19], exec
	s_cselect_b32 s37, s39, s43
	s_cselect_b32 s62, s38, s42
	s_ashr_i32 s23, s22, 31
	s_lshl_b64 s[40:41], s[22:23], 19
	v_readlane_b32 s46, v243, 51
	v_readlane_b32 s47, v243, 52
	s_add_u32 s40, s46, s40
	s_addc_u32 s41, s47, s41
	s_and_b64 s[46:47], s[18:19], exec
	s_cselect_b32 s23, s41, s45
	s_cselect_b32 s63, s40, s44
	s_add_u32 s42, s42, 0x40080
	s_addc_u32 s43, s43, 0
	s_add_u32 s66, s44, 0x100
	v_mov_b32_e32 v0, 0
	s_addc_u32 s67, s45, 0
	s_mov_b32 s68, -2
	v_mov_b32_e32 v1, v0
	v_pk_mov_b32 v[2:3], v[0:1], v[0:1]
	v_pk_mov_b32 v[4:5], v[0:1], v[0:1]
	v_pk_mov_b32 v[6:7], v[0:1], v[0:1]
	v_pk_mov_b32 v[8:9], v[0:1], v[0:1]
	v_pk_mov_b32 v[10:11], v[0:1], v[0:1]
	v_pk_mov_b32 v[12:13], v[0:1], v[0:1]
	v_pk_mov_b32 v[14:15], v[0:1], v[0:1]
	v_pk_mov_b32 v[16:17], v[0:1], v[0:1]
	v_pk_mov_b32 v[18:19], v[0:1], v[0:1]
	v_pk_mov_b32 v[20:21], v[0:1], v[0:1]
	v_pk_mov_b32 v[22:23], v[0:1], v[0:1]
	v_pk_mov_b32 v[24:25], v[0:1], v[0:1]
	v_pk_mov_b32 v[26:27], v[0:1], v[0:1]
	v_pk_mov_b32 v[28:29], v[0:1], v[0:1]
	v_pk_mov_b32 v[30:31], v[0:1], v[0:1]
	v_pk_mov_b32 v[32:33], v[0:1], v[0:1]
	v_pk_mov_b32 v[34:35], v[0:1], v[0:1]
	v_pk_mov_b32 v[36:37], v[0:1], v[0:1]
	v_pk_mov_b32 v[38:39], v[0:1], v[0:1]
	v_pk_mov_b32 v[40:41], v[0:1], v[0:1]
	v_pk_mov_b32 v[42:43], v[0:1], v[0:1]
	v_pk_mov_b32 v[44:45], v[0:1], v[0:1]
	v_pk_mov_b32 v[46:47], v[0:1], v[0:1]
	v_pk_mov_b32 v[48:49], v[0:1], v[0:1]
	v_pk_mov_b32 v[50:51], v[0:1], v[0:1]
	v_pk_mov_b32 v[52:53], v[0:1], v[0:1]
	v_pk_mov_b32 v[54:55], v[0:1], v[0:1]
	v_pk_mov_b32 v[56:57], v[0:1], v[0:1]
	v_pk_mov_b32 v[58:59], v[0:1], v[0:1]
	v_pk_mov_b32 v[60:61], v[0:1], v[0:1]
	v_pk_mov_b32 v[62:63], v[0:1], v[0:1]
	v_pk_mov_b32 v[64:65], v[0:1], v[0:1]
	v_pk_mov_b32 v[66:67], v[0:1], v[0:1]
	v_pk_mov_b32 v[68:69], v[0:1], v[0:1]
	v_pk_mov_b32 v[70:71], v[0:1], v[0:1]
	v_pk_mov_b32 v[72:73], v[0:1], v[0:1]
	v_pk_mov_b32 v[74:75], v[0:1], v[0:1]
	v_pk_mov_b32 v[76:77], v[0:1], v[0:1]
	v_pk_mov_b32 v[78:79], v[0:1], v[0:1]
	v_pk_mov_b32 v[80:81], v[0:1], v[0:1]
	v_pk_mov_b32 v[82:83], v[0:1], v[0:1]
	v_pk_mov_b32 v[84:85], v[0:1], v[0:1]
	v_pk_mov_b32 v[86:87], v[0:1], v[0:1]
	v_pk_mov_b32 v[88:89], v[0:1], v[0:1]
	v_pk_mov_b32 v[90:91], v[0:1], v[0:1]
	v_pk_mov_b32 v[92:93], v[0:1], v[0:1]
	v_pk_mov_b32 v[94:95], v[0:1], v[0:1]
	v_pk_mov_b32 v[96:97], v[0:1], v[0:1]
	v_pk_mov_b32 v[98:99], v[0:1], v[0:1]
	v_pk_mov_b32 v[100:101], v[0:1], v[0:1]
	v_pk_mov_b32 v[102:103], v[0:1], v[0:1]
	v_pk_mov_b32 v[104:105], v[0:1], v[0:1]
	v_pk_mov_b32 v[106:107], v[0:1], v[0:1]
	v_pk_mov_b32 v[108:109], v[0:1], v[0:1]
	v_pk_mov_b32 v[110:111], v[0:1], v[0:1]
	v_pk_mov_b32 v[112:113], v[0:1], v[0:1]
	v_pk_mov_b32 v[114:115], v[0:1], v[0:1]
	v_pk_mov_b32 v[116:117], v[0:1], v[0:1]
	v_pk_mov_b32 v[118:119], v[0:1], v[0:1]
	v_pk_mov_b32 v[120:121], v[0:1], v[0:1]
	v_pk_mov_b32 v[122:123], v[0:1], v[0:1]
	v_pk_mov_b32 v[124:125], v[0:1], v[0:1]
	v_pk_mov_b32 v[126:127], v[0:1], v[0:1]

; template <class Epi, class Sched>
; __device__ __forceinline__ void gemm_phase(const int WID_, PG8_LAS unsigned char* lds, const Sched& S, const Epi& E) {
;     ...
; #pragma unroll
;         for (int a = 0; a < 2; ++a)
; #pragma unroll
;             for (int b = 0; b < 2; ++b)
; #pragma unroll
;                 for (int m = 0; m < 4; ++m)
; #pragma unroll
;                     for (int n = 0; n < 2; ++n) acc[a][b][m][n] = (f32x4){0.f, 0.f, 0.f, 0.f};
;         cur = nxt; cA = nA; cB = nB; ++ui;
.LBB0_1891:
	v_mov_b32_e32 v0, 0
	s_mov_b32 s41, 0
	s_mov_b64 s[52:53], -1
	s_mov_b64 s[60:61], 0
	v_mov_b32_e32 v1, v0
	v_pk_mov_b32 v[2:3], v[0:1], v[0:1]
	v_pk_mov_b32 v[4:5], v[0:1], v[0:1]
	v_pk_mov_b32 v[6:7], v[0:1], v[0:1]
	v_pk_mov_b32 v[8:9], v[0:1], v[0:1]
	v_pk_mov_b32 v[10:11], v[0:1], v[0:1]
	v_pk_mov_b32 v[12:13], v[0:1], v[0:1]
	v_pk_mov_b32 v[14:15], v[0:1], v[0:1]
	v_pk_mov_b32 v[16:17], v[0:1], v[0:1]
	v_pk_mov_b32 v[18:19], v[0:1], v[0:1]
	v_pk_mov_b32 v[20:21], v[0:1], v[0:1]
	v_pk_mov_b32 v[22:23], v[0:1], v[0:1]
	v_pk_mov_b32 v[24:25], v[0:1], v[0:1]
	v_pk_mov_b32 v[26:27], v[0:1], v[0:1]
	v_pk_mov_b32 v[28:29], v[0:1], v[0:1]
	v_pk_mov_b32 v[30:31], v[0:1], v[0:1]
	v_pk_mov_b32 v[32:33], v[0:1], v[0:1]
	v_pk_mov_b32 v[34:35], v[0:1], v[0:1]
	v_pk_mov_b32 v[36:37], v[0:1], v[0:1]
	v_pk_mov_b32 v[38:39], v[0:1], v[0:1]
	v_pk_mov_b32 v[40:41], v[0:1], v[0:1]
	v_pk_mov_b32 v[42:43], v[0:1], v[0:1]
	v_pk_mov_b32 v[44:45], v[0:1], v[0:1]
	v_pk_mov_b32 v[46:47], v[0:1], v[0:1]
	v_pk_mov_b32 v[48:49], v[0:1], v[0:1]
	v_pk_mov_b32 v[50:51], v[0:1], v[0:1]
	v_pk_mov_b32 v[52:53], v[0:1], v[0:1]
	v_pk_mov_b32 v[54:55], v[0:1], v[0:1]
	v_pk_mov_b32 v[56:57], v[0:1], v[0:1]
	v_pk_mov_b32 v[58:59], v[0:1], v[0:1]
	v_pk_mov_b32 v[60:61], v[0:1], v[0:1]
	v_pk_mov_b32 v[62:63], v[0:1], v[0:1]
	v_pk_mov_b32 v[64:65], v[0:1], v[0:1]
	v_pk_mov_b32 v[66:67], v[0:1], v[0:1]
	v_pk_mov_b32 v[68:69], v[0:1], v[0:1]
	v_pk_mov_b32 v[70:71], v[0:1], v[0:1]
	v_pk_mov_b32 v[72:73], v[0:1], v[0:1]
	v_pk_mov_b32 v[74:75], v[0:1], v[0:1]
	v_pk_mov_b32 v[76:77], v[0:1], v[0:1]
	v_pk_mov_b32 v[78:79], v[0:1], v[0:1]
	v_pk_mov_b32 v[80:81], v[0:1], v[0:1]
	v_pk_mov_b32 v[82:83], v[0:1], v[0:1]
	v_pk_mov_b32 v[84:85], v[0:1], v[0:1]
	v_pk_mov_b32 v[86:87], v[0:1], v[0:1]
	v_pk_mov_b32 v[88:89], v[0:1], v[0:1]
	v_pk_mov_b32 v[90:91], v[0:1], v[0:1]
	v_pk_mov_b32 v[92:93], v[0:1], v[0:1]
	v_pk_mov_b32 v[94:95], v[0:1], v[0:1]
	v_pk_mov_b32 v[96:97], v[0:1], v[0:1]
	v_pk_mov_b32 v[98:99], v[0:1], v[0:1]
	v_pk_mov_b32 v[100:101], v[0:1], v[0:1]
	v_pk_mov_b32 v[102:103], v[0:1], v[0:1]
	v_pk_mov_b32 v[104:105], v[0:1], v[0:1]
	v_pk_mov_b32 v[106:107], v[0:1], v[0:1]
	v_pk_mov_b32 v[108:109], v[0:1], v[0:1]
	v_pk_mov_b32 v[110:111], v[0:1], v[0:1]
	v_pk_mov_b32 v[112:113], v[0:1], v[0:1]
	v_pk_mov_b32 v[114:115], v[0:1], v[0:1]
	v_pk_mov_b32 v[116:117], v[0:1], v[0:1]
	v_pk_mov_b32 v[118:119], v[0:1], v[0:1]
	v_pk_mov_b32 v[120:121], v[0:1], v[0:1]
	v_pk_mov_b32 v[122:123], v[0:1], v[0:1]
	v_pk_mov_b32 v[124:125], v[0:1], v[0:1]
	v_pk_mov_b32 v[126:127], v[0:1], v[0:1]

; template <class Epi, class Sched>
; __device__ __forceinline__ void gemm_phase(const int WID_, PG8_LAS unsigned char* lds, const Sched& S, const Epi& E) {
;     ...
; #pragma unroll
;         for (int a = 0; a < 2; ++a)
; #pragma unroll
;             for (int b = 0; b < 2; ++b)
; #pragma unroll
;                 for (int m = 0; m < 4; ++m)
; #pragma unroll
;                     for (int n = 0; n < 2; ++n) acc[a][b][m][n] = (f32x4){0.f, 0.f, 0.f, 0.f};
;         cur = nxt; cA = nA; cB = nB; ++ui;
.LBB0_1927:
	v_mov_b32_e32 v0, 0
	s_mov_b32 s43, 0
	s_mov_b64 s[48:49], -1
	s_mov_b64 s[50:51], 0
	v_mov_b32_e32 v1, v0
	v_pk_mov_b32 v[2:3], v[0:1], v[0:1]
	v_pk_mov_b32 v[4:5], v[0:1], v[0:1]
	v_pk_mov_b32 v[6:7], v[0:1], v[0:1]
	v_pk_mov_b32 v[8:9], v[0:1], v[0:1]
	v_pk_mov_b32 v[10:11], v[0:1], v[0:1]
	v_pk_mov_b32 v[12:13], v[0:1], v[0:1]
	v_pk_mov_b32 v[14:15], v[0:1], v[0:1]
	v_pk_mov_b32 v[16:17], v[0:1], v[0:1]
	v_pk_mov_b32 v[18:19], v[0:1], v[0:1]
	v_pk_mov_b32 v[20:21], v[0:1], v[0:1]
	v_pk_mov_b32 v[22:23], v[0:1], v[0:1]
	v_pk_mov_b32 v[24:25], v[0:1], v[0:1]
	v_pk_mov_b32 v[26:27], v[0:1], v[0:1]
	v_pk_mov_b32 v[28:29], v[0:1], v[0:1]
	v_pk_mov_b32 v[30:31], v[0:1], v[0:1]
	v_pk_mov_b32 v[32:33], v[0:1], v[0:1]
	v_pk_mov_b32 v[34:35], v[0:1], v[0:1]
	v_pk_mov_b32 v[36:37], v[0:1], v[0:1]
	v_pk_mov_b32 v[38:39], v[0:1], v[0:1]
	v_pk_mov_b32 v[40:41], v[0:1], v[0:1]
	v_pk_mov_b32 v[42:43], v[0:1], v[0:1]
	v_pk_mov_b32 v[44:45], v[0:1], v[0:1]
	v_pk_mov_b32 v[46:47], v[0:1], v[0:1]
	v_pk_mov_b32 v[48:49], v[0:1], v[0:1]
	v_pk_mov_b32 v[50:51], v[0:1], v[0:1]
	v_pk_mov_b32 v[52:53], v[0:1], v[0:1]
	v_pk_mov_b32 v[54:55], v[0:1], v[0:1]
	v_pk_mov_b32 v[56:57], v[0:1], v[0:1]
	v_pk_mov_b32 v[58:59], v[0:1], v[0:1]
	v_pk_mov_b32 v[60:61], v[0:1], v[0:1]
	v_pk_mov_b32 v[62:63], v[0:1], v[0:1]
	v_pk_mov_b32 v[64:65], v[0:1], v[0:1]
	v_pk_mov_b32 v[66:67], v[0:1], v[0:1]
	v_pk_mov_b32 v[68:69], v[0:1], v[0:1]
	v_pk_mov_b32 v[70:71], v[0:1], v[0:1]
	v_pk_mov_b32 v[72:73], v[0:1], v[0:1]
	v_pk_mov_b32 v[74:75], v[0:1], v[0:1]
	v_pk_mov_b32 v[76:77], v[0:1], v[0:1]
	v_pk_mov_b32 v[78:79], v[0:1], v[0:1]
	v_pk_mov_b32 v[80:81], v[0:1], v[0:1]
	v_pk_mov_b32 v[82:83], v[0:1], v[0:1]
	v_pk_mov_b32 v[84:85], v[0:1], v[0:1]
	v_pk_mov_b32 v[86:87], v[0:1], v[0:1]
	v_pk_mov_b32 v[88:89], v[0:1], v[0:1]
	v_pk_mov_b32 v[90:91], v[0:1], v[0:1]
	v_pk_mov_b32 v[92:93], v[0:1], v[0:1]
	v_pk_mov_b32 v[94:95], v[0:1], v[0:1]
	v_pk_mov_b32 v[96:97], v[0:1], v[0:1]
	v_pk_mov_b32 v[98:99], v[0:1], v[0:1]
	v_pk_mov_b32 v[100:101], v[0:1], v[0:1]
	v_pk_mov_b32 v[102:103], v[0:1], v[0:1]
	v_pk_mov_b32 v[104:105], v[0:1], v[0:1]
	v_pk_mov_b32 v[106:107], v[0:1], v[0:1]
	v_pk_mov_b32 v[108:109], v[0:1], v[0:1]
	v_pk_mov_b32 v[110:111], v[0:1], v[0:1]
	v_pk_mov_b32 v[112:113], v[0:1], v[0:1]
	v_pk_mov_b32 v[114:115], v[0:1], v[0:1]
	v_pk_mov_b32 v[116:117], v[0:1], v[0:1]
	v_pk_mov_b32 v[118:119], v[0:1], v[0:1]
	v_pk_mov_b32 v[120:121], v[0:1], v[0:1]
	v_pk_mov_b32 v[122:123], v[0:1], v[0:1]
	v_pk_mov_b32 v[124:125], v[0:1], v[0:1]
	v_pk_mov_b32 v[126:127], v[0:1], v[0:1]

; #define PG8_WAIT_V(n) asm volatile("s_waitcnt vmcnt(" #n ")" ::: "memory")
; template <class Epi, class Sched>
; __device__ __forceinline__ void gemm_phase(const int WID_, PG8_LAS unsigned char* lds, const Sched& S, const Epi& E) {
;     ...
;         const bool has_next = S.next(ui + 1, nxt);
;         const char* nA = has_next ? S.aptr(nxt) : cA; const char* nB = has_next ? S.bptr(nxt) : cB;
;         if (has_next) PG8_GOFF(vgn, nxt); else { if constexpr (GA) { _Pragma("unroll") for (int h_ = 0; h_ < 2; ++h_) _Pragma("unroll") for (int i_ = 0; i_ < 2; ++i_) vgn[h_][i_] = vgc[h_][i_]; } }
;         for (int t = 0; t < nt; t += 2) {
;             const bool last = (t == nt - 2);
;             const char* a1 = cA + (size_t)(t + 1) * kstep;
;             const char* a2 = last ? nA : cA + (size_t)(t + 2) * kstep; const char* b2 = last ? nB : cB + (size_t)(t + 2) * kstep;
;             const char* a3 = a2 + kstep; const char* b3 = b2 + kstep;
;             PG8_LDB(B0, 0, 0); PG8_LDB(B1, 0, 1); PG8_SCHED; PG8_LDA(At, 0, 0); PG8_STAGE_A(PG8_SA(1, 1), a1 + hstepA, 1, false);
;             PG8_WAIT_V(8); PG8_WAIT_L(0); PG8_BAR; PG8_MMA(0, 0, At, B0); PG8_MMA(0, 1, At, B1); PG8_BAR; PG8_SCHED;
;             PG8_LDA(At, 0, 1); PG8_STAGE(PG8_SB(0, 0), b2, voffB); PG8_STAGE(PG8_SB(0, 1), b2 + hstepB, voffB); PG8_STAGE_A(PG8_SA(0, 0), a2, 0, last);
;             PG8_WAIT_V(8); PG8_WAIT_L(0); PG8_BAR; PG8_MMA(1, 0, At, B0); PG8_MMA(1, 1, At, B1); PG8_BAR; PG8_SCHED;
;             PG8_LDB(B0, 1, 0); PG8_LDB(B1, 1, 1); PG8_SCHED; PG8_LDA(At, 1, 0); PG8_STAGE_A(PG8_SA(0, 1), a2 + hstepA, 1, last);
;             PG8_WAIT_V(8); PG8_WAIT_L(0); PG8_BAR; PG8_MMA(0, 0, At, B0); PG8_MMA(0, 1, At, B1); PG8_BAR; PG8_SCHED;
;             PG8_LDA(At, 1, 1); PG8_STAGE(PG8_SB(1, 0), b3, voffB); PG8_STAGE(PG8_SB(1, 1), b3 + hstepB, voffB); PG8_STAGE_A(PG8_SA(1, 0), a3, 0, last);
;             PG8_WAIT_V(8); PG8_WAIT_L(0); PG8_BAR; PG8_MMA(1, 0, At, B0); PG8_MMA(1, 1, At, B1); PG8_BAR; PG8_SCHED;
;         }
;         if (wr == 0) PG8_BAR;
;         E(acc, cur, wr, wc, fr, fq);
;         if (!has_next) break;
; #pragma unroll
;         for (int a = 0; a < 2; ++a)
; #pragma unroll
;             for (int b = 0; b < 2; ++b)
; #pragma unroll
;                 for (int m = 0; m < 4; ++m)
; #pragma unroll
;                     for (int n = 0; n < 2; ++n) acc[a][b][m][n] = (f32x4){0.f, 0.f, 0.f, 0.f};
.LBB0_2035:
	s_ashr_i32 s11, s10, 31
	s_lshl_b64 s[12:13], s[10:11], 19
	s_add_u32 s9, s26, s12
	s_addc_u32 s11, s27, s13
	s_and_b64 s[12:13], s[14:15], exec
	s_cselect_b32 s13, s11, s19
	s_cselect_b32 s12, s9, s18
	s_ashr_i32 s9, s8, 31
	s_lshl_b64 s[22:23], s[8:9], 19
	s_add_u32 s9, s54, s22
	s_addc_u32 s11, s55, s23
	s_and_b64 s[14:15], s[14:15], exec
	s_cselect_b32 s15, s11, s21
	s_cselect_b32 s14, s9, s20
	s_add_u32 s18, s18, 0x40080
	s_addc_u32 s19, s19, 0
	s_add_u32 s9, s20, 0x100
	v_mov_b32_e32 v0, 0
	s_addc_u32 s11, s21, 0
	s_mov_b32 s63, -2
	v_mov_b32_e32 v1, v0
	v_pk_mov_b32 v[2:3], v[0:1], v[0:1]
	v_pk_mov_b32 v[4:5], v[0:1], v[0:1]
	v_pk_mov_b32 v[6:7], v[0:1], v[0:1]
	v_pk_mov_b32 v[8:9], v[0:1], v[0:1]
	v_pk_mov_b32 v[10:11], v[0:1], v[0:1]
	v_pk_mov_b32 v[12:13], v[0:1], v[0:1]
	v_pk_mov_b32 v[14:15], v[0:1], v[0:1]
	v_pk_mov_b32 v[16:17], v[0:1], v[0:1]
	v_pk_mov_b32 v[18:19], v[0:1], v[0:1]
	v_pk_mov_b32 v[20:21], v[0:1], v[0:1]
	v_pk_mov_b32 v[22:23], v[0:1], v[0:1]
	v_pk_mov_b32 v[24:25], v[0:1], v[0:1]
	v_pk_mov_b32 v[26:27], v[0:1], v[0:1]
	v_pk_mov_b32 v[28:29], v[0:1], v[0:1]
	v_pk_mov_b32 v[30:31], v[0:1], v[0:1]
	v_pk_mov_b32 v[32:33], v[0:1], v[0:1]
	v_pk_mov_b32 v[34:35], v[0:1], v[0:1]
	v_pk_mov_b32 v[36:37], v[0:1], v[0:1]
	v_pk_mov_b32 v[38:39], v[0:1], v[0:1]
	v_pk_mov_b32 v[40:41], v[0:1], v[0:1]
	v_pk_mov_b32 v[42:43], v[0:1], v[0:1]
	v_pk_mov_b32 v[44:45], v[0:1], v[0:1]
	v_pk_mov_b32 v[46:47], v[0:1], v[0:1]
	v_pk_mov_b32 v[48:49], v[0:1], v[0:1]
	v_pk_mov_b32 v[50:51], v[0:1], v[0:1]
	v_pk_mov_b32 v[52:53], v[0:1], v[0:1]
	v_pk_mov_b32 v[54:55], v[0:1], v[0:1]
	v_pk_mov_b32 v[56:57], v[0:1], v[0:1]
	v_pk_mov_b32 v[58:59], v[0:1], v[0:1]
	v_pk_mov_b32 v[60:61], v[0:1], v[0:1]
	v_pk_mov_b32 v[62:63], v[0:1], v[0:1]
	v_pk_mov_b32 v[64:65], v[0:1], v[0:1]
	v_pk_mov_b32 v[66:67], v[0:1], v[0:1]
	v_pk_mov_b32 v[68:69], v[0:1], v[0:1]
	v_pk_mov_b32 v[70:71], v[0:1], v[0:1]
	v_pk_mov_b32 v[72:73], v[0:1], v[0:1]
	v_pk_mov_b32 v[74:75], v[0:1], v[0:1]
	v_pk_mov_b32 v[76:77], v[0:1], v[0:1]
	v_pk_mov_b32 v[78:79], v[0:1], v[0:1]
	v_pk_mov_b32 v[80:81], v[0:1], v[0:1]
	v_pk_mov_b32 v[82:83], v[0:1], v[0:1]
	v_pk_mov_b32 v[84:85], v[0:1], v[0:1]
	v_pk_mov_b32 v[86:87], v[0:1], v[0:1]
	v_pk_mov_b32 v[88:89], v[0:1], v[0:1]
	v_pk_mov_b32 v[90:91], v[0:1], v[0:1]
	v_pk_mov_b32 v[92:93], v[0:1], v[0:1]
	v_pk_mov_b32 v[94:95], v[0:1], v[0:1]
	v_pk_mov_b32 v[96:97], v[0:1], v[0:1]
	v_pk_mov_b32 v[98:99], v[0:1], v[0:1]
	v_pk_mov_b32 v[100:101], v[0:1], v[0:1]
	v_pk_mov_b32 v[102:103], v[0:1], v[0:1]
	v_pk_mov_b32 v[104:105], v[0:1], v[0:1]
	v_pk_mov_b32 v[106:107], v[0:1], v[0:1]
	v_pk_mov_b32 v[108:109], v[0:1], v[0:1]
	v_pk_mov_b32 v[110:111], v[0:1], v[0:1]
	v_pk_mov_b32 v[112:113], v[0:1], v[0:1]
	v_pk_mov_b32 v[114:115], v[0:1], v[0:1]
	v_pk_mov_b32 v[116:117], v[0:1], v[0:1]
	v_pk_mov_b32 v[118:119], v[0:1], v[0:1]
	v_pk_mov_b32 v[120:121], v[0:1], v[0:1]
	v_pk_mov_b32 v[122:123], v[0:1], v[0:1]
	v_pk_mov_b32 v[124:125], v[0:1], v[0:1]
	v_pk_mov_b32 v[126:127], v[0:1], v[0:1]

; #define PG8_WAIT_V(n) asm volatile("s_waitcnt vmcnt(" #n ")" ::: "memory")
; template <class Epi, class Sched>
; __device__ __forceinline__ void gemm_phase(const int WID_, PG8_LAS unsigned char* lds, const Sched& S, const Epi& E) {
;     ...
;         const bool has_next = S.next(ui + 1, nxt);
;         const char* nA = has_next ? S.aptr(nxt) : cA; const char* nB = has_next ? S.bptr(nxt) : cB;
;         if (has_next) PG8_GOFF(vgn, nxt); else { if constexpr (GA) { _Pragma("unroll") for (int h_ = 0; h_ < 2; ++h_) _Pragma("unroll") for (int i_ = 0; i_ < 2; ++i_) vgn[h_][i_] = vgc[h_][i_]; } }
;         for (int t = 0; t < nt; t += 2) {
;             const bool last = (t == nt - 2);
;             const char* a1 = cA + (size_t)(t + 1) * kstep;
;             const char* a2 = last ? nA : cA + (size_t)(t + 2) * kstep; const char* b2 = last ? nB : cB + (size_t)(t + 2) * kstep;
;             const char* a3 = a2 + kstep; const char* b3 = b2 + kstep;
;             PG8_LDB(B0, 0, 0); PG8_LDB(B1, 0, 1); PG8_SCHED; PG8_LDA(At, 0, 0); PG8_STAGE_A(PG8_SA(1, 1), a1 + hstepA, 1, false);
;             PG8_WAIT_V(8); PG8_WAIT_L(0); PG8_BAR; PG8_MMA(0, 0, At, B0); PG8_MMA(0, 1, At, B1); PG8_BAR; PG8_SCHED;
;             PG8_LDA(At, 0, 1); PG8_STAGE(PG8_SB(0, 0), b2, voffB); PG8_STAGE(PG8_SB(0, 1), b2 + hstepB, voffB); PG8_STAGE_A(PG8_SA(0, 0), a2, 0, last);
;             PG8_WAIT_V(8); PG8_WAIT_L(0); PG8_BAR; PG8_MMA(1, 0, At, B0); PG8_MMA(1, 1, At, B1); PG8_BAR; PG8_SCHED;
;             PG8_LDB(B0, 1, 0); PG8_LDB(B1, 1, 1); PG8_SCHED; PG8_LDA(At, 1, 0); PG8_STAGE_A(PG8_SA(0, 1), a2 + hstepA, 1, last);
;             PG8_WAIT_V(8); PG8_WAIT_L(0); PG8_BAR; PG8_MMA(0, 0, At, B0); PG8_MMA(0, 1, At, B1); PG8_BAR; PG8_SCHED;
;             PG8_LDA(At, 1, 1); PG8_STAGE(PG8_SB(1, 0), b3, voffB); PG8_STAGE(PG8_SB(1, 1), b3 + hstepB, voffB); PG8_STAGE_A(PG8_SA(1, 0), a3, 0, last);
;             PG8_WAIT_V(8); PG8_WAIT_L(0); PG8_BAR; PG8_MMA(1, 0, At, B0); PG8_MMA(1, 1, At, B1); PG8_BAR; PG8_SCHED;
;         }
;         if (wr == 0) PG8_BAR;
;         E(acc, cur, wr, wc, fr, fq);
;         if (!has_next) break;
; #pragma unroll
;         for (int a = 0; a < 2; ++a)
; #pragma unroll
;             for (int b = 0; b < 2; ++b)
; #pragma unroll
;                 for (int m = 0; m < 4; ++m)
; #pragma unroll
;                     for (int n = 0; n < 2; ++n) acc[a][b][m][n] = (f32x4){0.f, 0.f, 0.f, 0.f};
.LBB0_2069:
	s_ashr_i32 s15, s14, 31
	s_lshl_b64 s[16:17], s[14:15], 19
	s_add_u32 s13, s92, s16
	s_addc_u32 s15, s93, s17
	s_and_b64 s[16:17], s[18:19], exec
	s_cselect_b32 s17, s15, s23
	s_cselect_b32 s16, s13, s22
	s_ashr_i32 s13, s12, 31
	s_lshl_b64 s[80:81], s[12:13], 19
	s_add_u32 s13, s48, s80
	s_addc_u32 s15, s49, s81
	s_and_b64 s[18:19], s[18:19], exec
	s_cselect_b32 s19, s15, s79
	s_cselect_b32 s18, s13, s78
	s_add_u32 s22, s22, 0x40080
	s_addc_u32 s23, s23, 0
	s_add_u32 s13, s78, 0x100
	v_mov_b32_e32 v0, 0
	s_addc_u32 s15, s79, 0
	s_mov_b32 vcc_lo, -2
	v_mov_b32_e32 v1, v0
	v_pk_mov_b32 v[2:3], v[0:1], v[0:1]
	v_pk_mov_b32 v[4:5], v[0:1], v[0:1]
	v_pk_mov_b32 v[6:7], v[0:1], v[0:1]
	v_pk_mov_b32 v[8:9], v[0:1], v[0:1]
	v_pk_mov_b32 v[10:11], v[0:1], v[0:1]
	v_pk_mov_b32 v[12:13], v[0:1], v[0:1]
	v_pk_mov_b32 v[14:15], v[0:1], v[0:1]
	v_pk_mov_b32 v[16:17], v[0:1], v[0:1]
	v_pk_mov_b32 v[18:19], v[0:1], v[0:1]
	v_pk_mov_b32 v[20:21], v[0:1], v[0:1]
	v_pk_mov_b32 v[22:23], v[0:1], v[0:1]
	v_pk_mov_b32 v[24:25], v[0:1], v[0:1]
	v_pk_mov_b32 v[26:27], v[0:1], v[0:1]
	v_pk_mov_b32 v[28:29], v[0:1], v[0:1]
	v_pk_mov_b32 v[30:31], v[0:1], v[0:1]
	v_pk_mov_b32 v[32:33], v[0:1], v[0:1]
	v_pk_mov_b32 v[34:35], v[0:1], v[0:1]
	v_pk_mov_b32 v[36:37], v[0:1], v[0:1]
	v_pk_mov_b32 v[38:39], v[0:1], v[0:1]
	v_pk_mov_b32 v[40:41], v[0:1], v[0:1]
	v_pk_mov_b32 v[42:43], v[0:1], v[0:1]
	v_pk_mov_b32 v[44:45], v[0:1], v[0:1]
	v_pk_mov_b32 v[46:47], v[0:1], v[0:1]
	v_pk_mov_b32 v[48:49], v[0:1], v[0:1]
	v_pk_mov_b32 v[50:51], v[0:1], v[0:1]
	v_pk_mov_b32 v[52:53], v[0:1], v[0:1]
	v_pk_mov_b32 v[54:55], v[0:1], v[0:1]
	v_pk_mov_b32 v[56:57], v[0:1], v[0:1]
	v_pk_mov_b32 v[58:59], v[0:1], v[0:1]
	v_pk_mov_b32 v[60:61], v[0:1], v[0:1]
	v_pk_mov_b32 v[62:63], v[0:1], v[0:1]
	v_pk_mov_b32 v[64:65], v[0:1], v[0:1]
	v_pk_mov_b32 v[66:67], v[0:1], v[0:1]
	v_pk_mov_b32 v[68:69], v[0:1], v[0:1]
	v_pk_mov_b32 v[70:71], v[0:1], v[0:1]
	v_pk_mov_b32 v[72:73], v[0:1], v[0:1]
	v_pk_mov_b32 v[74:75], v[0:1], v[0:1]
	v_pk_mov_b32 v[76:77], v[0:1], v[0:1]
	v_pk_mov_b32 v[78:79], v[0:1], v[0:1]
	v_pk_mov_b32 v[80:81], v[0:1], v[0:1]
	v_pk_mov_b32 v[82:83], v[0:1], v[0:1]
	v_pk_mov_b32 v[84:85], v[0:1], v[0:1]
	v_pk_mov_b32 v[86:87], v[0:1], v[0:1]
	v_pk_mov_b32 v[88:89], v[0:1], v[0:1]
	v_pk_mov_b32 v[90:91], v[0:1], v[0:1]
	v_pk_mov_b32 v[92:93], v[0:1], v[0:1]
	v_pk_mov_b32 v[94:95], v[0:1], v[0:1]
	v_pk_mov_b32 v[96:97], v[0:1], v[0:1]
	v_pk_mov_b32 v[98:99], v[0:1], v[0:1]
	v_pk_mov_b32 v[100:101], v[0:1], v[0:1]
	v_pk_mov_b32 v[102:103], v[0:1], v[0:1]
	v_pk_mov_b32 v[104:105], v[0:1], v[0:1]
	v_pk_mov_b32 v[106:107], v[0:1], v[0:1]
	v_pk_mov_b32 v[108:109], v[0:1], v[0:1]
	v_pk_mov_b32 v[110:111], v[0:1], v[0:1]
	v_pk_mov_b32 v[112:113], v[0:1], v[0:1]
	v_pk_mov_b32 v[114:115], v[0:1], v[0:1]
	v_pk_mov_b32 v[116:117], v[0:1], v[0:1]
	v_pk_mov_b32 v[118:119], v[0:1], v[0:1]
	v_pk_mov_b32 v[120:121], v[0:1], v[0:1]
	v_pk_mov_b32 v[122:123], v[0:1], v[0:1]
	v_pk_mov_b32 v[124:125], v[0:1], v[0:1]
	v_pk_mov_b32 v[126:127], v[0:1], v[0:1]

; #define PG8_WAIT_V(n) asm volatile("s_waitcnt vmcnt(" #n ")" ::: "memory")
; template <class Epi, class Sched>
; __device__ __forceinline__ void gemm_phase(const int WID_, PG8_LAS unsigned char* lds, const Sched& S, const Epi& E) {
;     ...
;         const bool has_next = S.next(ui + 1, nxt);
;         const char* nA = has_next ? S.aptr(nxt) : cA; const char* nB = has_next ? S.bptr(nxt) : cB;
;         if (has_next) PG8_GOFF(vgn, nxt); else { if constexpr (GA) { _Pragma("unroll") for (int h_ = 0; h_ < 2; ++h_) _Pragma("unroll") for (int i_ = 0; i_ < 2; ++i_) vgn[h_][i_] = vgc[h_][i_]; } }
;         for (int t = 0; t < nt; t += 2) {
;             const bool last = (t == nt - 2);
;             const char* a1 = cA + (size_t)(t + 1) * kstep;
;             const char* a2 = last ? nA : cA + (size_t)(t + 2) * kstep; const char* b2 = last ? nB : cB + (size_t)(t + 2) * kstep;
;             const char* a3 = a2 + kstep; const char* b3 = b2 + kstep;
;             PG8_LDB(B0, 0, 0); PG8_LDB(B1, 0, 1); PG8_SCHED; PG8_LDA(At, 0, 0); PG8_STAGE_A(PG8_SA(1, 1), a1 + hstepA, 1, false);
;             PG8_WAIT_V(8); PG8_WAIT_L(0); PG8_BAR; PG8_MMA(0, 0, At, B0); PG8_MMA(0, 1, At, B1); PG8_BAR; PG8_SCHED;
;             PG8_LDA(At, 0, 1); PG8_STAGE(PG8_SB(0, 0), b2, voffB); PG8_STAGE(PG8_SB(0, 1), b2 + hstepB, voffB); PG8_STAGE_A(PG8_SA(0, 0), a2, 0, last);
;             PG8_WAIT_V(8); PG8_WAIT_L(0); PG8_BAR; PG8_MMA(1, 0, At, B0); PG8_MMA(1, 1, At, B1); PG8_BAR; PG8_SCHED;
;             PG8_LDB(B0, 1, 0); PG8_LDB(B1, 1, 1); PG8_SCHED; PG8_LDA(At, 1, 0); PG8_STAGE_A(PG8_SA(0, 1), a2 + hstepA, 1, last);
;             PG8_WAIT_V(8); PG8_WAIT_L(0); PG8_BAR; PG8_MMA(0, 0, At, B0); PG8_MMA(0, 1, At, B1); PG8_BAR; PG8_SCHED;
;             PG8_LDA(At, 1, 1); PG8_STAGE(PG8_SB(1, 0), b3, voffB); PG8_STAGE(PG8_SB(1, 1), b3 + hstepB, voffB); PG8_STAGE_A(PG8_SA(1, 0), a3, 0, last);
;             PG8_WAIT_V(8); PG8_WAIT_L(0); PG8_BAR; PG8_MMA(1, 0, At, B0); PG8_MMA(1, 1, At, B1); PG8_BAR; PG8_SCHED;
;         }
;         if (wr == 0) PG8_BAR;
;         E(acc, cur, wr, wc, fr, fq);
;         if (!has_next) break;
; #pragma unroll
;         for (int a = 0; a < 2; ++a)
; #pragma unroll
;             for (int b = 0; b < 2; ++b)
; #pragma unroll
;                 for (int m = 0; m < 4; ++m)
; #pragma unroll
;                     for (int n = 0; n < 2; ++n) acc[a][b][m][n] = (f32x4){0.f, 0.f, 0.f, 0.f};
.LBB0_2119:
	s_ashr_i32 s11, s10, 31
	s_lshl_b64 s[12:13], s[10:11], 19
	s_add_u32 s9, s30, s12
	s_addc_u32 s11, s31, s13
	s_and_b64 s[12:13], s[14:15], exec
	s_cselect_b32 s13, s11, s19
	s_cselect_b32 s12, s9, s18
	s_ashr_i32 s9, s8, 31
	s_lshl_b64 s[22:23], s[8:9], 19
	s_add_u32 s9, s33, s22
	s_addc_u32 s11, s44, s23
	s_and_b64 s[14:15], s[14:15], exec
	s_cselect_b32 s15, s11, s21
	s_cselect_b32 s14, s9, s20
	s_add_u32 s18, s18, 0x40080
	s_addc_u32 s19, s19, 0
	s_add_u32 s9, s20, 0x100
	v_mov_b32_e32 v0, 0
	s_addc_u32 s11, s21, 0
	s_mov_b32 s79, -2
	v_mov_b32_e32 v1, v0
	v_pk_mov_b32 v[2:3], v[0:1], v[0:1]
	v_pk_mov_b32 v[4:5], v[0:1], v[0:1]
	v_pk_mov_b32 v[6:7], v[0:1], v[0:1]
	v_pk_mov_b32 v[8:9], v[0:1], v[0:1]
	v_pk_mov_b32 v[10:11], v[0:1], v[0:1]
	v_pk_mov_b32 v[12:13], v[0:1], v[0:1]
	v_pk_mov_b32 v[14:15], v[0:1], v[0:1]
	v_pk_mov_b32 v[16:17], v[0:1], v[0:1]
	v_pk_mov_b32 v[18:19], v[0:1], v[0:1]
	v_pk_mov_b32 v[20:21], v[0:1], v[0:1]
	v_pk_mov_b32 v[22:23], v[0:1], v[0:1]
	v_pk_mov_b32 v[24:25], v[0:1], v[0:1]
	v_pk_mov_b32 v[26:27], v[0:1], v[0:1]
	v_pk_mov_b32 v[28:29], v[0:1], v[0:1]
	v_pk_mov_b32 v[30:31], v[0:1], v[0:1]
	v_pk_mov_b32 v[32:33], v[0:1], v[0:1]
	v_pk_mov_b32 v[34:35], v[0:1], v[0:1]
	v_pk_mov_b32 v[36:37], v[0:1], v[0:1]
	v_pk_mov_b32 v[38:39], v[0:1], v[0:1]
	v_pk_mov_b32 v[40:41], v[0:1], v[0:1]
	v_pk_mov_b32 v[42:43], v[0:1], v[0:1]
	v_pk_mov_b32 v[44:45], v[0:1], v[0:1]
	v_pk_mov_b32 v[46:47], v[0:1], v[0:1]
	v_pk_mov_b32 v[48:49], v[0:1], v[0:1]
	v_pk_mov_b32 v[50:51], v[0:1], v[0:1]
	v_pk_mov_b32 v[52:53], v[0:1], v[0:1]
	v_pk_mov_b32 v[54:55], v[0:1], v[0:1]
	v_pk_mov_b32 v[56:57], v[0:1], v[0:1]
	v_pk_mov_b32 v[58:59], v[0:1], v[0:1]
	v_pk_mov_b32 v[60:61], v[0:1], v[0:1]
	v_pk_mov_b32 v[62:63], v[0:1], v[0:1]
	v_pk_mov_b32 v[64:65], v[0:1], v[0:1]
	v_pk_mov_b32 v[66:67], v[0:1], v[0:1]
	v_pk_mov_b32 v[68:69], v[0:1], v[0:1]
	v_pk_mov_b32 v[70:71], v[0:1], v[0:1]
	v_pk_mov_b32 v[72:73], v[0:1], v[0:1]
	v_pk_mov_b32 v[74:75], v[0:1], v[0:1]
	v_pk_mov_b32 v[76:77], v[0:1], v[0:1]
	v_pk_mov_b32 v[78:79], v[0:1], v[0:1]
	v_pk_mov_b32 v[80:81], v[0:1], v[0:1]
	v_pk_mov_b32 v[82:83], v[0:1], v[0:1]
	v_pk_mov_b32 v[84:85], v[0:1], v[0:1]
	v_pk_mov_b32 v[86:87], v[0:1], v[0:1]
	v_pk_mov_b32 v[88:89], v[0:1], v[0:1]
	v_pk_mov_b32 v[90:91], v[0:1], v[0:1]
	v_pk_mov_b32 v[92:93], v[0:1], v[0:1]
	v_pk_mov_b32 v[94:95], v[0:1], v[0:1]
	v_pk_mov_b32 v[96:97], v[0:1], v[0:1]
	v_pk_mov_b32 v[98:99], v[0:1], v[0:1]
	v_pk_mov_b32 v[100:101], v[0:1], v[0:1]
	v_pk_mov_b32 v[102:103], v[0:1], v[0:1]
	v_pk_mov_b32 v[104:105], v[0:1], v[0:1]
	v_pk_mov_b32 v[106:107], v[0:1], v[0:1]
	v_pk_mov_b32 v[108:109], v[0:1], v[0:1]
	v_pk_mov_b32 v[110:111], v[0:1], v[0:1]
	v_pk_mov_b32 v[112:113], v[0:1], v[0:1]
	v_pk_mov_b32 v[114:115], v[0:1], v[0:1]
	v_pk_mov_b32 v[116:117], v[0:1], v[0:1]
	v_pk_mov_b32 v[118:119], v[0:1], v[0:1]
	v_pk_mov_b32 v[120:121], v[0:1], v[0:1]
	v_pk_mov_b32 v[122:123], v[0:1], v[0:1]
	v_pk_mov_b32 v[124:125], v[0:1], v[0:1]
	v_pk_mov_b32 v[126:127], v[0:1], v[0:1]

; __device__ __forceinline__ void router_ph(const int WID_, const bf16* __restrict__ x3, const float* __restrict__ nw, const float* __restrict__ wrg, const float* __restrict__ brg, ...
;     ...
;     for (int m = tile * 256 + wv; m < tile * 256 + 256; m += 8) {
;         float h[16]; float s = 0.f;
; #pragma unroll
;         for (int j = 0; j < 2; ++j) { const unsigned wd[4] = {nx[j].x, nx[j].y, nx[j].z, nx[j].w};
; #pragma unroll
;             for (int q = 0; q < 4; ++q) { const float lo = __builtin_bit_cast(float, wd[q] << 16), hi = __builtin_bit_cast(float, wd[q] & 0xffff0000u); h[8 * j + 2 * q] = lo; h[8 * j + 2 * q + 1] = hi; s += lo * lo + hi * hi; } }
;         { const int mn = min(m + 8, tile * 256 + 248 + wv); const uint4* xr = (const uint4*)(x3 + (size_t)mn * D);
; #pragma unroll
;           for (int j = 0; j < 2; ++j) nx[j] = xr[lane + 64 * j]; }
;         s = wave_sum(s);
;         const float rs = rsqrtf(s * (1.f / D) + 1e-6f);
;         float l1[4] = {0.f, 0.f, 0.f, 0.f};
; #pragma unroll
;         for (int j = 0; j < 2; ++j) {
;             const int k0 = (lane + 64 * j) * 8;
;             const float4 ga = gw[2 * j], gb = gw[2 * j + 1];
;             h[8 * j] *= rs * ga.x; h[8 * j + 1] *= rs * ga.y; h[8 * j + 2] *= rs * ga.z; h[8 * j + 3] *= rs * ga.w;
;             h[8 * j + 4] *= rs * gb.x; h[8 * j + 5] *= rs * gb.y; h[8 * j + 6] *= rs * gb.z; h[8 * j + 7] *= rs * gb.w;
; #pragma unroll
;             for (int e = 0; e < 8; ++e) { const h4 w = *(const h4*)(wg16 + (k0 + e) * 4); const float x = h[8 * j + e];
;                 l1[0] += x * (float)w[0]; l1[1] += x * (float)w[1]; l1[2] += x * (float)w[2]; l1[3] += x * (float)w[3]; }
;         }
; #pragma unroll
;         for (int i = 0; i < 4; ++i) l1[i] = wave_sum(l1[i]) + brg_l[i];
.LBB0_2145:
	v_and_b32_e32 v90, 0xffff0000, v16
	v_and_b32_e32 v92, 0xffff0000, v17
	v_lshlrev_b32_e32 v59, 16, v16
	v_mul_f32_e32 v14, v90, v90
	v_lshlrev_b32_e32 v91, 16, v17
	v_mul_f32_e32 v16, v92, v92
	v_fmac_f32_e32 v14, v59, v59
	v_fmac_f32_e32 v16, v91, v91
	v_and_b32_e32 v94, 0xffff0000, v18
	v_add_f32_e32 v14, v16, v14
	v_lshlrev_b32_e32 v93, 16, v18
	v_mul_f32_e32 v16, v94, v94
	v_fmac_f32_e32 v16, v93, v93
	v_and_b32_e32 v96, 0xffff0000, v19
	v_add_f32_e32 v14, v16, v14
	v_lshlrev_b32_e32 v95, 16, v19
	v_mul_f32_e32 v16, v96, v96
	v_and_b32_e32 v85, 0xffff0000, v13
	v_and_b32_e32 v84, 0xffff0000, v12
	v_fmac_f32_e32 v16, v95, v95
	v_lshlrev_b32_e32 v27, 16, v13
	v_lshlrev_b32_e32 v26, 16, v12
	v_pk_mul_f32 v[12:13], v[84:85], v[84:85]
	v_add_f32_e32 v14, v16, v14
	v_pk_fma_f32 v[16:17], v[26:27], v[26:27], v[12:13]
	v_and_b32_e32 v86, 0xffff0000, v2
	v_add_f32_e32 v14, v16, v14
	v_add_f32_e32 v88, v17, v14
	v_and_b32_e32 v14, 0xffff0000, v15
	v_lshlrev_b32_e32 v15, 16, v15
	v_lshlrev_b32_e32 v87, 16, v2
	v_mov_b32_e32 v82, v14
	v_mov_b32_e32 v83, v86
	v_mov_b32_e32 v80, v15
	v_mov_b32_e32 v81, v87
	v_pk_mul_f32 v[82:83], v[82:83], v[82:83]
	s_add_i32 s4, s44, 16
	v_pk_fma_f32 v[80:81], v[80:81], v[80:81], v[82:83]
	s_min_i32 s4, s4, s33
	v_add_f32_e32 v2, v81, v88
	v_add_f32_e32 v2, v80, v2
	v_mov_b32_e32 v80, 0
	s_ashr_i32 s5, s4, 31
	v_add_f32_dpp v2, v2, v2 quad_perm:[1,0,3,2] row_mask:0xf bank_mask:0xf bound_ctrl:1
	s_lshl_b64 s[4:5], s[4:5], 11
	v_lshl_add_u64 v[12:13], v[10:11], 0, s[4:5]
	v_add_f32_dpp v2, v2, v2 quad_perm:[2,3,0,1] row_mask:0xf bank_mask:0xf bound_ctrl:1
	ds_read_b128 v[16:19], v21 offset:256
	ds_read_b128 v[22:25], v52 offset:256
	ds_read_b128 v[60:63], v53 offset:256
	ds_read_b128 v[64:67], v54 offset:256
	ds_read_b128 v[68:71], v55 offset:256
	ds_read_b128 v[72:75], v56 offset:256
	ds_read_b128 v[76:79], v57 offset:256
	v_add_f32_dpp v2, v2, v2 row_half_mirror row_mask:0xf bank_mask:0xf bound_ctrl:1
	s_add_i32 s5, 0, 0x12100
	s_waitcnt lgkmcnt(0)
	v_cvt_f32_f16_sdwa v89, v77 dst_sel:DWORD dst_unused:UNUSED_PAD src0_sel:WORD_1
	v_add_f32_dpp v2, v2, v2 row_mirror row_mask:0xf bank_mask:0xf bound_ctrl:1
	v_cvt_f32_f16_sdwa v88, v79 dst_sel:DWORD dst_unused:UNUSED_PAD src0_sel:WORD_1
	s_nop 0
	v_mov_b32_dpp v80, v2 row_bcast:15 row_mask:0xa bank_mask:0xf
	v_add_f32_e32 v2, v2, v80
	v_mov_b32_e32 v80, 0
	s_nop 1
	v_mov_b32_dpp v80, v2 row_bcast:31 row_mask:0xc bank_mask:0xf
	v_add_f32_e32 v2, v2, v80
	s_nop 0
	v_readlane_b32 s4, v2, 63
	s_nop 1
	v_fma_f32 v2, s4, v196, v194
	v_mul_f32_e32 v80, 0x4b800000, v2
	v_cmp_gt_f32_e32 vcc, s64, v2
	s_nop 1
	v_cndmask_b32_e32 v2, v2, v80, vcc
	v_rsq_f32_e32 v2, v2
	ds_read_b128 v[80:83], v58 offset:256
	v_mul_f32_e32 v97, 0x45800000, v2
	v_cndmask_b32_e32 v2, v2, v97, vcc
	v_mul_f32_e32 v97, v29, v2
	v_mul_f32_e32 v97, v97, v59
	v_mul_f32_e32 v59, v31, v2
	v_mul_f32_e32 v90, v59, v90
	v_mul_f32_e32 v59, v30, v2
	v_mul_f32_e32 v91, v59, v91
	v_mul_f32_e32 v59, v3, v2
	v_mul_f32_e32 v92, v59, v92
	v_mul_f32_e32 v59, v33, v2
	v_mul_f32_e32 v93, v59, v93
	v_mul_f32_e32 v59, v32, v2
	v_mul_f32_e32 v94, v59, v94
	v_mul_f32_e32 v59, v6, v2
	v_mul_f32_e32 v95, v59, v95
	v_mul_f32_e32 v59, v7, v2
	v_mul_f32_e32 v96, v59, v96
	v_fma_mix_f32 v59, v97, v16, 0 op_sel_hi:[0,1,0]
	v_fma_mix_f32 v16, v97, v16, 0 op_sel:[0,1,0] op_sel_hi:[0,1,0]
	v_fma_mix_f32 v16, v90, v18, v16 op_sel:[0,1,0] op_sel_hi:[0,1,0]
	v_fma_mix_f32 v16, v91, v22, v16 op_sel:[0,1,0] op_sel_hi:[0,1,0]
	v_fma_mix_f32 v16, v92, v24, v16 op_sel:[0,1,0] op_sel_hi:[0,1,0]
	v_fma_mix_f32 v98, v97, v17, 0 op_sel_hi:[0,1,0]
	v_fma_mix_f32 v17, v97, v17, 0 op_sel:[0,1,0] op_sel_hi:[0,1,0]
	v_fma_mix_f32 v16, v93, v60, v16 op_sel:[0,1,0] op_sel_hi:[0,1,0]
	v_fma_mix_f32 v17, v90, v19, v17 op_sel:[0,1,0] op_sel_hi:[0,1,0]
	v_fma_mix_f32 v16, v94, v62, v16 op_sel:[0,1,0] op_sel_hi:[0,1,0]
	v_fma_mix_f32 v59, v90, v18, v59 op_sel_hi:[0,1,0]
	v_fma_mix_f32 v17, v91, v23, v17 op_sel:[0,1,0] op_sel_hi:[0,1,0]
	v_fma_mix_f32 v16, v95, v64, v16 op_sel:[0,1,0] op_sel_hi:[0,1,0]
	v_fma_mix_f32 v18, v90, v19, v98 op_sel_hi:[0,1,0]
	v_fma_mix_f32 v19, v91, v22, v59 op_sel_hi:[0,1,0]
	v_fma_mix_f32 v17, v92, v25, v17 op_sel:[0,1,0] op_sel_hi:[0,1,0]
	v_fma_mix_f32 v22, v96, v66, v16 op_sel:[0,1,0] op_sel_hi:[0,1,0]
	v_mul_f32_e32 v16, v8, v2
	v_fma_mix_f32 v18, v91, v23, v18 op_sel_hi:[0,1,0]
	v_fma_mix_f32 v19, v92, v24, v19 op_sel_hi:[0,1,0]
	v_fma_mix_f32 v17, v93, v61, v17 op_sel:[0,1,0] op_sel_hi:[0,1,0]
	v_mul_f32_e32 v98, v16, v26
	v_mul_f32_e32 v16, v9, v2
	v_fma_mix_f32 v18, v92, v25, v18 op_sel_hi:[0,1,0]
	v_fma_mix_f32 v19, v93, v60, v19 op_sel_hi:[0,1,0]
	v_fma_mix_f32 v17, v94, v63, v17 op_sel:[0,1,0] op_sel_hi:[0,1,0]
	v_mul_f32_e32 v84, v16, v84
	v_mul_f32_e32 v16, v35, v2
	v_fma_mix_f32 v18, v93, v61, v18 op_sel_hi:[0,1,0]
	v_fma_mix_f32 v19, v94, v62, v19 op_sel_hi:[0,1,0]
	v_fma_mix_f32 v17, v95, v65, v17 op_sel:[0,1,0] op_sel_hi:[0,1,0]
	v_mul_f32_e32 v99, v16, v27
	v_mul_f32_e32 v16, v34, v2
	v_fma_mix_f32 v18, v94, v63, v18 op_sel_hi:[0,1,0]
	v_fma_mix_f32 v19, v95, v64, v19 op_sel_hi:[0,1,0]
	v_fma_mix_f32 v23, v96, v67, v17 op_sel:[0,1,0] op_sel_hi:[0,1,0]
	v_mul_f32_e32 v85, v16, v85
	v_pk_mul_f32 v[16:17], v[0:1], v[2:3] op_sel_hi:[1,0]
	v_fma_mix_f32 v18, v95, v65, v18 op_sel_hi:[0,1,0]
	v_fma_mix_f32 v19, v96, v66, v19 op_sel_hi:[0,1,0]
	v_pk_mul_f32 v[26:27], v[16:17], v[86:87]
	v_pk_mul_f32 v[16:17], v[4:5], v[2:3] op_sel_hi:[1,0]
	v_fma_mix_f32 v18, v96, v67, v18 op_sel_hi:[0,1,0]
	v_pk_mul_f32 v[24:25], v[16:17], v[14:15]
	v_fma_mix_f32 v14, v98, v68, v19 op_sel_hi:[0,1,0]
	v_fma_mix_f32 v15, v98, v68, v22 op_sel:[0,1,0] op_sel_hi:[0,1,0]
	v_fma_mix_f32 v16, v98, v69, v18 op_sel_hi:[0,1,0]
	v_fma_mix_f32 v17, v98, v69, v23 op_sel:[0,1,0] op_sel_hi:[0,1,0]
	v_fma_mix_f32 v14, v84, v70, v14 op_sel_hi:[0,1,0]
	v_fma_mix_f32 v15, v84, v70, v15 op_sel:[0,1,0] op_sel_hi:[0,1,0]
	v_fma_mix_f32 v16, v84, v71, v16 op_sel_hi:[0,1,0]
	v_fma_mix_f32 v17, v84, v71, v17 op_sel:[0,1,0] op_sel_hi:[0,1,0]
	v_fma_mix_f32 v14, v99, v72, v14 op_sel_hi:[0,1,0]
	v_fma_mix_f32 v15, v99, v72, v15 op_sel:[0,1,0] op_sel_hi:[0,1,0]
	v_fma_mix_f32 v16, v99, v73, v16 op_sel_hi:[0,1,0]
	v_fma_mix_f32 v17, v99, v73, v17 op_sel:[0,1,0] op_sel_hi:[0,1,0]
	v_fma_mix_f32 v14, v85, v74, v14 op_sel_hi:[0,1,0]
	v_fma_mix_f32 v22, v85, v74, v15 op_sel:[0,1,0] op_sel_hi:[0,1,0]
	v_fma_mix_f32 v23, v85, v75, v16 op_sel_hi:[0,1,0]
	v_fma_mix_f32 v16, v85, v75, v17 op_sel:[0,1,0] op_sel_hi:[0,1,0]
	v_fma_mix_f32 v18, v27, v76, v14 op_sel_hi:[0,1,0]
	v_pk_mul_f32 v[14:15], v[26:27], v[88:89]
	v_cvt_f32_f16_sdwa v17, v76 dst_sel:DWORD dst_unused:UNUSED_PAD src0_sel:WORD_1
	v_add_f32_e32 v15, v15, v16
	v_cvt_f32_f16_sdwa v16, v78 dst_sel:DWORD dst_unused:UNUSED_PAD src0_sel:WORD_1
	v_fma_mix_f32 v59, v26, v78, v18 op_sel_hi:[0,1,0]
	v_cvt_f32_f16_e32 v19, v77
	v_cvt_f32_f16_e32 v18, v79
	v_pk_mul_f32 v[16:17], v[26:27], v[16:17]
	s_waitcnt lgkmcnt(0)
; __device__ __forceinline__ void router_ph(const int WID_, const bf16* __restrict__ x3, const float* __restrict__ nw, const float* __restrict__ wrg, const float* __restrict__ brg, ...
;     ...
;         int grp = 0; float best = l1[0];
; #pragma unroll
;         for (int i = 1; i < 4; ++i) if (l1[i] > best) { best = l1[i]; grp = i; }
;         float se = 0.f;
; #pragma unroll
;         for (int i = 0; i < 4; ++i) se += __expf(l1[i] - best);
;         const float g1 = 1.f / se;
;         float l2[8] = {};
;         const _Float16* we = we16 + (size_t)grp * D * 8;
; #pragma unroll
;         for (int j = 0; j < 2; ++j) {
;             const int k0 = (lane + 64 * j) * 8;
; #pragma unroll
;             for (int e = 0; e < 8; ++e) { const float x = h[8 * j + e]; const h8 w = *(const h8*)(we + (k0 + e) * 8);
; #pragma unroll
;                 for (int q = 0; q < 8; ++q) l2[q] += x * (float)w[q]; }
;         }
	v_fma_mix_f32 v59, v25, v80, v59 op_sel_hi:[0,1,0]
	v_add_f32_e32 v17, v17, v22
	v_add_f32_e32 v22, v16, v17
	v_pk_mul_f32 v[16:17], v[26:27], v[18:19]
	v_cvt_f32_f16_sdwa v19, v81 dst_sel:DWORD dst_unused:UNUSED_PAD src0_sel:WORD_1
	v_cvt_f32_f16_sdwa v18, v83 dst_sel:DWORD dst_unused:UNUSED_PAD src0_sel:WORD_1
	v_add_f32_e32 v17, v17, v23
	v_add_f32_e32 v23, v16, v17
	v_add_f32_e32 v16, v14, v15
	v_pk_mul_f32 v[14:15], v[24:25], v[18:19]
	v_cvt_f32_f16_sdwa v17, v80 dst_sel:DWORD dst_unused:UNUSED_PAD src0_sel:WORD_1
	v_add_f32_e32 v15, v15, v16
	v_cvt_f32_f16_sdwa v16, v82 dst_sel:DWORD dst_unused:UNUSED_PAD src0_sel:WORD_1
	v_cvt_f32_f16_e32 v19, v81
	v_cvt_f32_f16_e32 v18, v83
	v_fma_mix_f32 v59, v24, v82, v59 op_sel_hi:[0,1,0]
	v_pk_mul_f32 v[16:17], v[24:25], v[16:17]
	s_nop 0
	v_add_f32_e32 v17, v17, v22
	v_add_f32_e32 v22, v16, v17
	v_pk_mul_f32 v[16:17], v[24:25], v[18:19]
	v_add_f32_e32 v19, v14, v15
	v_add_f32_dpp v14, v59, v59 quad_perm:[1,0,3,2] row_mask:0xf bank_mask:0xf bound_ctrl:1
	v_mov_b32_e32 v15, 0
	v_add_f32_e32 v17, v17, v23
	v_add_f32_dpp v14, v14, v14 quad_perm:[2,3,0,1] row_mask:0xf bank_mask:0xf bound_ctrl:1
	v_add_f32_e32 v18, v16, v17
	v_mov_b32_e32 v23, 0
	v_add_f32_dpp v14, v14, v14 row_half_mirror row_mask:0xf bank_mask:0xf bound_ctrl:1
	s_nop 1
	v_add_f32_dpp v14, v14, v14 row_mirror row_mask:0xf bank_mask:0xf bound_ctrl:1
	s_nop 1
	v_mov_b32_dpp v15, v14 row_bcast:15 row_mask:0xa bank_mask:0xf
	v_add_f32_e32 v14, v14, v15
	v_mov_b32_e32 v15, 0
	s_nop 1
	v_mov_b32_dpp v15, v14 row_bcast:31 row_mask:0xc bank_mask:0xf
	v_add_f32_e32 v14, v14, v15
	v_mov_b32_e32 v15, 0
	v_readlane_b32 s4, v14, 63
	v_add_f32_dpp v14, v22, v22 quad_perm:[1,0,3,2] row_mask:0xf bank_mask:0xf bound_ctrl:1
	s_nop 1
	v_add_f32_dpp v14, v14, v14 quad_perm:[2,3,0,1] row_mask:0xf bank_mask:0xf bound_ctrl:1
	s_nop 1
	v_add_f32_dpp v14, v14, v14 row_half_mirror row_mask:0xf bank_mask:0xf bound_ctrl:1
	s_nop 1
	v_add_f32_dpp v14, v14, v14 row_mirror row_mask:0xf bank_mask:0xf bound_ctrl:1
	s_nop 1
	v_mov_b32_dpp v15, v14 row_bcast:15 row_mask:0xa bank_mask:0xf
	v_add_f32_e32 v22, v14, v15
	v_mov_b32_e32 v14, s5
	ds_read_b128 v[14:17], v14
	v_mov_b32_dpp v23, v22 row_bcast:31 row_mask:0xc bank_mask:0xf
	v_add_f32_e32 v22, v22, v23
	s_nop 0
	v_readlane_b32 s5, v22, 63
	s_waitcnt lgkmcnt(0)
	s_nop 0
	v_pk_add_f32 v[22:23], s[4:5], v[14:15]
	v_add_f32_dpp v14, v18, v18 quad_perm:[1,0,3,2] row_mask:0xf bank_mask:0xf bound_ctrl:1
	v_mov_b32_e32 v15, 0
	s_nop 0
	v_add_f32_dpp v14, v14, v14 quad_perm:[2,3,0,1] row_mask:0xf bank_mask:0xf bound_ctrl:1
	s_nop 1
	v_add_f32_dpp v14, v14, v14 row_half_mirror row_mask:0xf bank_mask:0xf bound_ctrl:1
	s_nop 1
	v_add_f32_dpp v14, v14, v14 row_mirror row_mask:0xf bank_mask:0xf bound_ctrl:1
	s_nop 1
	v_mov_b32_dpp v15, v14 row_bcast:15 row_mask:0xa bank_mask:0xf
	v_add_f32_e32 v14, v14, v15
	v_mov_b32_e32 v15, 0
	s_nop 1
	v_mov_b32_dpp v15, v14 row_bcast:31 row_mask:0xc bank_mask:0xf
	v_add_f32_e32 v14, v14, v15
	v_mov_b32_e32 v15, 0
	v_readlane_b32 s4, v14, 63
	v_add_f32_dpp v14, v19, v19 quad_perm:[1,0,3,2] row_mask:0xf bank_mask:0xf bound_ctrl:1
	s_nop 0
	v_add_f32_e32 v59, s4, v16
	v_add_f32_dpp v14, v14, v14 quad_perm:[2,3,0,1] row_mask:0xf bank_mask:0xf bound_ctrl:1
	s_nop 1
	v_add_f32_dpp v14, v14, v14 row_half_mirror row_mask:0xf bank_mask:0xf bound_ctrl:1
	s_nop 1
	v_add_f32_dpp v14, v14, v14 row_mirror row_mask:0xf bank_mask:0xf bound_ctrl:1
	s_nop 1
	v_mov_b32_dpp v15, v14 row_bcast:15 row_mask:0xa bank_mask:0xf
	v_add_f32_e32 v14, v14, v15
	v_mov_b32_e32 v15, 0
	s_nop 1
	v_mov_b32_dpp v15, v14 row_bcast:31 row_mask:0xc bank_mask:0xf
	v_add_f32_e32 v14, v14, v15
	s_nop 0
	v_readlane_b32 s4, v14, 63
	s_nop 1
	v_add_f32_e32 v60, s4, v17
	v_cmp_gt_f32_e64 s[4:5], v23, v22
	s_nop 1
	v_cndmask_b32_e64 v14, v22, v23, s[4:5]
	v_cmp_gt_f32_e64 s[6:7], v59, v14
	s_nop 1
	v_cndmask_b32_e64 v61, v14, v59, s[6:7]
	v_cndmask_b32_e64 v14, 0, 1, s[4:5]
	s_and_b64 s[4:5], s[6:7], exec
	v_cmp_gt_f32_e32 vcc, v60, v61
	v_readfirstlane_b32 s4, v14
	s_cselect_b32 s6, 2, s4
	s_and_b64 s[4:5], vcc, exec
	s_cselect_b32 s49, 3, s6
	s_lshl_b32 s4, s49, 14
	s_add_i32 s48, s4, 0
	global_load_dwordx4 v[16:19], v[12:13], off
	s_nop 0
	global_load_dwordx4 v[12:15], v[12:13], off offset:1024
	v_add_u32_e32 v112, s48, v36
	ds_read_b128 v[132:135], v112 offset:8448
	v_add_u32_e32 v113, s48, v37
	ds_read_b128 v[136:139], v113 offset:8448
	v_add_u32_e32 v112, s48, v38
	ds_read_b128 v[140:143], v112 offset:8448
	v_add_u32_e32 v113, s48, v39
	ds_read_b128 v[144:147], v113 offset:8448
	v_add_u32_e32 v112, s48, v40
	ds_read_b128 v[148:151], v112 offset:8448
	v_add_u32_e32 v113, s48, v41
	ds_read_b128 v[152:155], v113 offset:8448
	v_add_u32_e32 v112, s48, v42
	ds_read_b128 v[156:159], v112 offset:8448
	v_add_u32_e32 v113, s48, v43
	ds_read_b128 v[160:163], v113 offset:8448
	v_add_u32_e32 v112, s48, v44
	ds_read_b128 v[164:167], v112 offset:8448
	v_add_u32_e32 v113, s48, v45
	ds_read_b128 v[168:171], v113 offset:8448
	v_add_u32_e32 v112, s48, v46
	ds_read_b128 v[172:175], v112 offset:8448
	v_add_u32_e32 v113, s48, v47
	ds_read_b128 v[176:179], v113 offset:8448
	s_waitcnt lgkmcnt(11)
	v_fma_mix_f32 v70, v97, v132, 0 op_sel_hi:[0,1,0]
	v_fma_mix_f32 v71, v97, v132, 0 op_sel:[0,1,0] op_sel_hi:[0,1,0]
	v_fma_mix_f32 v72, v97, v133, 0 op_sel_hi:[0,1,0]
	v_fma_mix_f32 v73, v97, v133, 0 op_sel:[0,1,0] op_sel_hi:[0,1,0]
	v_fma_mix_f32 v74, v97, v134, 0 op_sel_hi:[0,1,0]
	v_fma_mix_f32 v75, v97, v134, 0 op_sel:[0,1,0] op_sel_hi:[0,1,0]
	v_fma_mix_f32 v76, v97, v135, 0 op_sel_hi:[0,1,0]
	v_fma_mix_f32 v77, v97, v135, 0 op_sel:[0,1,0] op_sel_hi:[0,1,0]
	s_waitcnt lgkmcnt(10)
; __device__ __forceinline__ void router_ph(const int WID_, const bf16* __restrict__ x3, const float* __restrict__ nw, const float* __restrict__ wrg, const float* __restrict__ brg, ...
;     ...
;         float l2[8] = {};
;         const _Float16* we = we16 + (size_t)grp * D * 8;
; #pragma unroll
;         for (int j = 0; j < 2; ++j) {
;             const int k0 = (lane + 64 * j) * 8;
; #pragma unroll
;             for (int e = 0; e < 8; ++e) { const float x = h[8 * j + e]; const h8 w = *(const h8*)(we + (k0 + e) * 8);
; #pragma unroll
;                 for (int q = 0; q < 8; ++q) l2[q] += x * (float)w[q]; }
;         }
	v_fma_mix_f32 v70, v90, v136, v70 op_sel_hi:[0,1,0]
	v_fma_mix_f32 v71, v90, v136, v71 op_sel:[0,1,0] op_sel_hi:[0,1,0]
	v_fma_mix_f32 v72, v90, v137, v72 op_sel_hi:[0,1,0]
	v_fma_mix_f32 v73, v90, v137, v73 op_sel:[0,1,0] op_sel_hi:[0,1,0]
	v_fma_mix_f32 v74, v90, v138, v74 op_sel_hi:[0,1,0]
	v_fma_mix_f32 v75, v90, v138, v75 op_sel:[0,1,0] op_sel_hi:[0,1,0]
	v_fma_mix_f32 v76, v90, v139, v76 op_sel_hi:[0,1,0]
	v_fma_mix_f32 v77, v90, v139, v77 op_sel:[0,1,0] op_sel_hi:[0,1,0]
	s_waitcnt lgkmcnt(9)
	v_fma_mix_f32 v70, v91, v140, v70 op_sel_hi:[0,1,0]
	v_fma_mix_f32 v71, v91, v140, v71 op_sel:[0,1,0] op_sel_hi:[0,1,0]
	v_fma_mix_f32 v72, v91, v141, v72 op_sel_hi:[0,1,0]
	v_fma_mix_f32 v73, v91, v141, v73 op_sel:[0,1,0] op_sel_hi:[0,1,0]
	v_fma_mix_f32 v74, v91, v142, v74 op_sel_hi:[0,1,0]
	v_fma_mix_f32 v75, v91, v142, v75 op_sel:[0,1,0] op_sel_hi:[0,1,0]
	v_fma_mix_f32 v76, v91, v143, v76 op_sel_hi:[0,1,0]
	v_fma_mix_f32 v77, v91, v143, v77 op_sel:[0,1,0] op_sel_hi:[0,1,0]
	s_waitcnt lgkmcnt(8)
	v_fma_mix_f32 v70, v92, v144, v70 op_sel_hi:[0,1,0]
	v_fma_mix_f32 v71, v92, v144, v71 op_sel:[0,1,0] op_sel_hi:[0,1,0]
	v_fma_mix_f32 v72, v92, v145, v72 op_sel_hi:[0,1,0]
	v_fma_mix_f32 v73, v92, v145, v73 op_sel:[0,1,0] op_sel_hi:[0,1,0]
	v_fma_mix_f32 v74, v92, v146, v74 op_sel_hi:[0,1,0]
	v_fma_mix_f32 v75, v92, v146, v75 op_sel:[0,1,0] op_sel_hi:[0,1,0]
	v_fma_mix_f32 v76, v92, v147, v76 op_sel_hi:[0,1,0]
	v_fma_mix_f32 v77, v92, v147, v77 op_sel:[0,1,0] op_sel_hi:[0,1,0]
	v_add_u32_e32 v112, s48, v48
	ds_read_b128 v[180:183], v112 offset:8448
	v_add_u32_e32 v113, s48, v49
	ds_read_b128 v[184:187], v113 offset:8448
	v_add_u32_e32 v112, s48, v50
	ds_read_b128 v[188:191], v112 offset:8448
	v_add_u32_e32 v113, s48, v51
	ds_read_b128 v[108:111], v113 offset:8448
	s_waitcnt lgkmcnt(11)
	v_fma_mix_f32 v70, v93, v148, v70 op_sel_hi:[0,1,0]
	v_fma_mix_f32 v71, v93, v148, v71 op_sel:[0,1,0] op_sel_hi:[0,1,0]
	v_fma_mix_f32 v72, v93, v149, v72 op_sel_hi:[0,1,0]
	v_fma_mix_f32 v73, v93, v149, v73 op_sel:[0,1,0] op_sel_hi:[0,1,0]
	v_fma_mix_f32 v74, v93, v150, v74 op_sel_hi:[0,1,0]
	v_fma_mix_f32 v75, v93, v150, v75 op_sel:[0,1,0] op_sel_hi:[0,1,0]
	v_fma_mix_f32 v76, v93, v151, v76 op_sel_hi:[0,1,0]
	v_fma_mix_f32 v77, v93, v151, v77 op_sel:[0,1,0] op_sel_hi:[0,1,0]
	s_waitcnt lgkmcnt(10)
	v_fma_mix_f32 v70, v94, v152, v70 op_sel_hi:[0,1,0]
	v_fma_mix_f32 v71, v94, v152, v71 op_sel:[0,1,0] op_sel_hi:[0,1,0]
	v_fma_mix_f32 v72, v94, v153, v72 op_sel_hi:[0,1,0]
	v_fma_mix_f32 v73, v94, v153, v73 op_sel:[0,1,0] op_sel_hi:[0,1,0]
	v_fma_mix_f32 v74, v94, v154, v74 op_sel_hi:[0,1,0]
	v_fma_mix_f32 v75, v94, v154, v75 op_sel:[0,1,0] op_sel_hi:[0,1,0]
	v_fma_mix_f32 v76, v94, v155, v76 op_sel_hi:[0,1,0]
	v_fma_mix_f32 v77, v94, v155, v77 op_sel:[0,1,0] op_sel_hi:[0,1,0]
	s_waitcnt lgkmcnt(9)
	v_fma_mix_f32 v70, v95, v156, v70 op_sel_hi:[0,1,0]
	v_fma_mix_f32 v71, v95, v156, v71 op_sel:[0,1,0] op_sel_hi:[0,1,0]
	v_fma_mix_f32 v72, v95, v157, v72 op_sel_hi:[0,1,0]
	v_fma_mix_f32 v73, v95, v157, v73 op_sel:[0,1,0] op_sel_hi:[0,1,0]
	v_fma_mix_f32 v74, v95, v158, v74 op_sel_hi:[0,1,0]
	v_fma_mix_f32 v75, v95, v158, v75 op_sel:[0,1,0] op_sel_hi:[0,1,0]
	v_fma_mix_f32 v76, v95, v159, v76 op_sel_hi:[0,1,0]
	v_fma_mix_f32 v77, v95, v159, v77 op_sel:[0,1,0] op_sel_hi:[0,1,0]
	s_waitcnt lgkmcnt(8)
	v_fma_mix_f32 v70, v96, v160, v70 op_sel_hi:[0,1,0]
	v_fma_mix_f32 v71, v96, v160, v71 op_sel:[0,1,0] op_sel_hi:[0,1,0]
	v_fma_mix_f32 v72, v96, v161, v72 op_sel_hi:[0,1,0]
	v_fma_mix_f32 v73, v96, v161, v73 op_sel:[0,1,0] op_sel_hi:[0,1,0]
	v_fma_mix_f32 v74, v96, v162, v74 op_sel_hi:[0,1,0]
	v_fma_mix_f32 v75, v96, v162, v75 op_sel:[0,1,0] op_sel_hi:[0,1,0]
	v_fma_mix_f32 v76, v96, v163, v76 op_sel_hi:[0,1,0]
	v_fma_mix_f32 v77, v96, v163, v77 op_sel:[0,1,0] op_sel_hi:[0,1,0]
	s_waitcnt lgkmcnt(7)
	v_fma_mix_f32 v70, v98, v164, v70 op_sel_hi:[0,1,0]
	v_fma_mix_f32 v71, v98, v164, v71 op_sel:[0,1,0] op_sel_hi:[0,1,0]
	v_fma_mix_f32 v72, v98, v165, v72 op_sel_hi:[0,1,0]
	v_fma_mix_f32 v73, v98, v165, v73 op_sel:[0,1,0] op_sel_hi:[0,1,0]
	v_fma_mix_f32 v74, v98, v166, v74 op_sel_hi:[0,1,0]
	v_fma_mix_f32 v75, v98, v166, v75 op_sel:[0,1,0] op_sel_hi:[0,1,0]
	v_fma_mix_f32 v76, v98, v167, v76 op_sel_hi:[0,1,0]
	v_fma_mix_f32 v77, v98, v167, v77 op_sel:[0,1,0] op_sel_hi:[0,1,0]
	s_waitcnt lgkmcnt(6)
	v_fma_mix_f32 v70, v84, v168, v70 op_sel_hi:[0,1,0]
	v_fma_mix_f32 v71, v84, v168, v71 op_sel:[0,1,0] op_sel_hi:[0,1,0]
	v_fma_mix_f32 v72, v84, v169, v72 op_sel_hi:[0,1,0]
	v_fma_mix_f32 v73, v84, v169, v73 op_sel:[0,1,0] op_sel_hi:[0,1,0]
	v_fma_mix_f32 v74, v84, v170, v74 op_sel_hi:[0,1,0]
	v_fma_mix_f32 v75, v84, v170, v75 op_sel:[0,1,0] op_sel_hi:[0,1,0]
	v_fma_mix_f32 v76, v84, v171, v76 op_sel_hi:[0,1,0]
	v_fma_mix_f32 v77, v84, v171, v77 op_sel:[0,1,0] op_sel_hi:[0,1,0]
	s_waitcnt lgkmcnt(5)
	v_fma_mix_f32 v70, v99, v172, v70 op_sel_hi:[0,1,0]
	v_fma_mix_f32 v71, v99, v172, v71 op_sel:[0,1,0] op_sel_hi:[0,1,0]
	v_fma_mix_f32 v72, v99, v173, v72 op_sel_hi:[0,1,0]
	v_fma_mix_f32 v73, v99, v173, v73 op_sel:[0,1,0] op_sel_hi:[0,1,0]
	v_fma_mix_f32 v74, v99, v174, v74 op_sel_hi:[0,1,0]
	v_fma_mix_f32 v75, v99, v174, v75 op_sel:[0,1,0] op_sel_hi:[0,1,0]
	v_fma_mix_f32 v76, v99, v175, v76 op_sel_hi:[0,1,0]
	v_fma_mix_f32 v77, v99, v175, v77 op_sel:[0,1,0] op_sel_hi:[0,1,0]
	s_waitcnt lgkmcnt(4)
	v_fma_mix_f32 v70, v85, v176, v70 op_sel_hi:[0,1,0]
	v_fma_mix_f32 v71, v85, v176, v71 op_sel:[0,1,0] op_sel_hi:[0,1,0]
	v_fma_mix_f32 v72, v85, v177, v72 op_sel_hi:[0,1,0]
	v_fma_mix_f32 v73, v85, v177, v73 op_sel:[0,1,0] op_sel_hi:[0,1,0]
	v_fma_mix_f32 v74, v85, v178, v74 op_sel_hi:[0,1,0]
	v_fma_mix_f32 v75, v85, v178, v75 op_sel:[0,1,0] op_sel_hi:[0,1,0]
	v_fma_mix_f32 v76, v85, v179, v76 op_sel_hi:[0,1,0]
	v_fma_mix_f32 v77, v85, v179, v77 op_sel:[0,1,0] op_sel_hi:[0,1,0]
	s_waitcnt lgkmcnt(3)
; template <int CTRL, int ROWMASK> __device__ __forceinline__ float dppf_(float x) { return __builtin_bit_cast(float, __builtin_amdgcn_update_dpp(0, __builtin_bit_cast(int, x), CTRL, ROWMASK, 0xf, false)); }
; __device__ __forceinline__ float wave_sum(float v) {
;     v += dppf_<0xB1, 0xf>(v); v += dppf_<0x4E, 0xf>(v); v += dppf_<0x141, 0xf>(v); v += dppf_<0x140, 0xf>(v);
;     v += dppf_<0x142, 0xa>(v);
;     v += dppf_<0x143, 0xc>(v);
;     return __builtin_bit_cast(float, __builtin_amdgcn_readlane(__builtin_bit_cast(int, v), 63));
; }
; __device__ __forceinline__ void router_ph(const int WID_, const bf16* __restrict__ x3, const float* __restrict__ nw, const float* __restrict__ wrg, const float* __restrict__ brg, ...
;     ...
;         for (int i = 0; i < 8; ++i) l2[i] = wave_sum(l2[i]) + bre_l[grp * 8 + i];
	v_fma_mix_f32 v70, v27, v180, v70 op_sel_hi:[0,1,0]
	v_fma_mix_f32 v71, v27, v180, v71 op_sel:[0,1,0] op_sel_hi:[0,1,0]
	v_fma_mix_f32 v72, v27, v181, v72 op_sel_hi:[0,1,0]
	v_fma_mix_f32 v73, v27, v181, v73 op_sel:[0,1,0] op_sel_hi:[0,1,0]
	v_fma_mix_f32 v74, v27, v182, v74 op_sel_hi:[0,1,0]
	v_fma_mix_f32 v75, v27, v182, v75 op_sel:[0,1,0] op_sel_hi:[0,1,0]
	v_fma_mix_f32 v76, v27, v183, v76 op_sel_hi:[0,1,0]
	v_fma_mix_f32 v77, v27, v183, v77 op_sel:[0,1,0] op_sel_hi:[0,1,0]
	s_waitcnt lgkmcnt(2)
	v_fma_mix_f32 v70, v26, v184, v70 op_sel_hi:[0,1,0]
	v_fma_mix_f32 v71, v26, v184, v71 op_sel:[0,1,0] op_sel_hi:[0,1,0]
	v_fma_mix_f32 v72, v26, v185, v72 op_sel_hi:[0,1,0]
	v_fma_mix_f32 v73, v26, v185, v73 op_sel:[0,1,0] op_sel_hi:[0,1,0]
	v_fma_mix_f32 v74, v26, v186, v74 op_sel_hi:[0,1,0]
	v_fma_mix_f32 v75, v26, v186, v75 op_sel:[0,1,0] op_sel_hi:[0,1,0]
	v_fma_mix_f32 v76, v26, v187, v76 op_sel_hi:[0,1,0]
	v_fma_mix_f32 v77, v26, v187, v77 op_sel:[0,1,0] op_sel_hi:[0,1,0]
	s_waitcnt lgkmcnt(1)
	v_fma_mix_f32 v70, v25, v188, v70 op_sel_hi:[0,1,0]
	v_fma_mix_f32 v71, v25, v188, v71 op_sel:[0,1,0] op_sel_hi:[0,1,0]
	v_fma_mix_f32 v72, v25, v189, v72 op_sel_hi:[0,1,0]
	v_fma_mix_f32 v73, v25, v189, v73 op_sel:[0,1,0] op_sel_hi:[0,1,0]
	v_fma_mix_f32 v74, v25, v190, v74 op_sel_hi:[0,1,0]
	v_fma_mix_f32 v75, v25, v190, v75 op_sel:[0,1,0] op_sel_hi:[0,1,0]
	v_fma_mix_f32 v76, v25, v191, v76 op_sel_hi:[0,1,0]
	v_fma_mix_f32 v77, v25, v191, v77 op_sel:[0,1,0] op_sel_hi:[0,1,0]
	s_waitcnt lgkmcnt(0)
	v_fma_mix_f32 v70, v24, v108, v70 op_sel_hi:[0,1,0]
	v_fma_mix_f32 v71, v24, v108, v71 op_sel:[0,1,0] op_sel_hi:[0,1,0]
	v_fma_mix_f32 v72, v24, v109, v72 op_sel_hi:[0,1,0]
	v_fma_mix_f32 v73, v24, v109, v73 op_sel:[0,1,0] op_sel_hi:[0,1,0]
	v_fma_mix_f32 v74, v24, v110, v74 op_sel_hi:[0,1,0]
	v_fma_mix_f32 v75, v24, v110, v75 op_sel:[0,1,0] op_sel_hi:[0,1,0]
	v_fma_mix_f32 v76, v24, v111, v76 op_sel_hi:[0,1,0]
	v_fma_mix_f32 v77, v24, v111, v77 op_sel:[0,1,0] op_sel_hi:[0,1,0]
	v_mov_b32_e32 v26, v70
	v_mov_b32_e32 v27, v71
	v_mov_b32_e32 v62, v72
	v_mov_b32_e32 v63, v73
	v_mov_b32_e32 v65, v74
	v_mov_b32_e32 v64, v75
	v_mov_b32_e32 v66, v76
	v_mov_b32_e32 v24, v77
	v_add_f32_dpp v26, v26, v26 quad_perm:[1,0,3,2] row_mask:0xf bank_mask:0xf bound_ctrl:1
	v_add_f32_dpp v27, v27, v27 quad_perm:[1,0,3,2] row_mask:0xf bank_mask:0xf bound_ctrl:1
	v_add_f32_dpp v62, v62, v62 quad_perm:[1,0,3,2] row_mask:0xf bank_mask:0xf bound_ctrl:1
	v_add_f32_dpp v63, v63, v63 quad_perm:[1,0,3,2] row_mask:0xf bank_mask:0xf bound_ctrl:1
	v_add_f32_dpp v65, v65, v65 quad_perm:[1,0,3,2] row_mask:0xf bank_mask:0xf bound_ctrl:1
	v_add_f32_dpp v64, v64, v64 quad_perm:[1,0,3,2] row_mask:0xf bank_mask:0xf bound_ctrl:1
	v_add_f32_dpp v66, v66, v66 quad_perm:[1,0,3,2] row_mask:0xf bank_mask:0xf bound_ctrl:1
	v_add_f32_dpp v24, v24, v24 quad_perm:[1,0,3,2] row_mask:0xf bank_mask:0xf bound_ctrl:1
	v_add_f32_dpp v26, v26, v26 quad_perm:[2,3,0,1] row_mask:0xf bank_mask:0xf bound_ctrl:1
	v_add_f32_dpp v27, v27, v27 quad_perm:[2,3,0,1] row_mask:0xf bank_mask:0xf bound_ctrl:1
	v_add_f32_dpp v62, v62, v62 quad_perm:[2,3,0,1] row_mask:0xf bank_mask:0xf bound_ctrl:1
	v_add_f32_dpp v63, v63, v63 quad_perm:[2,3,0,1] row_mask:0xf bank_mask:0xf bound_ctrl:1
	v_add_f32_dpp v65, v65, v65 quad_perm:[2,3,0,1] row_mask:0xf bank_mask:0xf bound_ctrl:1
	v_add_f32_dpp v64, v64, v64 quad_perm:[2,3,0,1] row_mask:0xf bank_mask:0xf bound_ctrl:1
	v_add_f32_dpp v66, v66, v66 quad_perm:[2,3,0,1] row_mask:0xf bank_mask:0xf bound_ctrl:1
	v_add_f32_dpp v24, v24, v24 quad_perm:[2,3,0,1] row_mask:0xf bank_mask:0xf bound_ctrl:1
	v_add_f32_dpp v26, v26, v26 row_half_mirror row_mask:0xf bank_mask:0xf bound_ctrl:1
	v_add_f32_dpp v27, v27, v27 row_half_mirror row_mask:0xf bank_mask:0xf bound_ctrl:1
	v_add_f32_dpp v62, v62, v62 row_half_mirror row_mask:0xf bank_mask:0xf bound_ctrl:1
	v_add_f32_dpp v63, v63, v63 row_half_mirror row_mask:0xf bank_mask:0xf bound_ctrl:1
	v_add_f32_dpp v65, v65, v65 row_half_mirror row_mask:0xf bank_mask:0xf bound_ctrl:1
	v_add_f32_dpp v64, v64, v64 row_half_mirror row_mask:0xf bank_mask:0xf bound_ctrl:1
	v_add_f32_dpp v66, v66, v66 row_half_mirror row_mask:0xf bank_mask:0xf bound_ctrl:1
	v_add_f32_dpp v24, v24, v24 row_half_mirror row_mask:0xf bank_mask:0xf bound_ctrl:1
	v_add_f32_dpp v26, v26, v26 row_mirror row_mask:0xf bank_mask:0xf bound_ctrl:1
	v_add_f32_dpp v27, v27, v27 row_mirror row_mask:0xf bank_mask:0xf bound_ctrl:1
	v_add_f32_dpp v62, v62, v62 row_mirror row_mask:0xf bank_mask:0xf bound_ctrl:1
	v_add_f32_dpp v63, v63, v63 row_mirror row_mask:0xf bank_mask:0xf bound_ctrl:1
	v_add_f32_dpp v65, v65, v65 row_mirror row_mask:0xf bank_mask:0xf bound_ctrl:1
	v_add_f32_dpp v64, v64, v64 row_mirror row_mask:0xf bank_mask:0xf bound_ctrl:1
	v_add_f32_dpp v66, v66, v66 row_mirror row_mask:0xf bank_mask:0xf bound_ctrl:1
	v_add_f32_dpp v24, v24, v24 row_mirror row_mask:0xf bank_mask:0xf bound_ctrl:1
	v_mov_b32_e32 v100, 0
	v_mov_b32_e32 v101, 0
	v_mov_b32_e32 v102, 0
	v_mov_b32_e32 v103, 0
	v_mov_b32_e32 v104, 0
	v_mov_b32_e32 v105, 0
	v_mov_b32_e32 v106, 0
	v_mov_b32_e32 v107, 0
	v_mov_b32_dpp v100, v26 row_bcast:15 row_mask:0xa bank_mask:0xf
	v_mov_b32_dpp v101, v27 row_bcast:15 row_mask:0xa bank_mask:0xf
	v_mov_b32_dpp v102, v62 row_bcast:15 row_mask:0xa bank_mask:0xf
	v_mov_b32_dpp v103, v63 row_bcast:15 row_mask:0xa bank_mask:0xf
	v_mov_b32_dpp v104, v65 row_bcast:15 row_mask:0xa bank_mask:0xf
	v_mov_b32_dpp v105, v64 row_bcast:15 row_mask:0xa bank_mask:0xf
	v_mov_b32_dpp v106, v66 row_bcast:15 row_mask:0xa bank_mask:0xf
	v_mov_b32_dpp v107, v24 row_bcast:15 row_mask:0xa bank_mask:0xf
; __device__ __forceinline__ void router_ph(const int WID_, const bf16* __restrict__ x3, const float* __restrict__ nw, const float* __restrict__ wrg, const float* __restrict__ brg, ...
;     ...
;         for (int i = 0; i < 8; ++i) l2[i] = wave_sum(l2[i]) + bre_l[grp * 8 + i];
;         int i0 = 0; float v0 = l2[0];
; #pragma unroll
;         for (int i = 1; i < 8; ++i) if (l2[i] > v0) { v0 = l2[i]; i0 = i; }
;         int i1 = -1; float v1 = -3.0e38f;
; #pragma unroll
;         for (int i = 0; i < 8; ++i) if (i != i0 && l2[i] > v1) { v1 = l2[i]; i1 = i; }
;         const float e1 = __expf(v1 - v0), inv = 1.f / (1.f + e1);
;         if (lane == 0) {
;             const int ea = grp * 8 + i0, eb = grp * 8 + i1;
;             mb.tok_e[2 * m] = ea; mb.tok_e[2 * m + 1] = eb; mb.tok_rs[m] = rs;
;             mb.tok_g[2 * m] = g1 * inv; mb.tok_g[2 * m + 1] = g1 * e1 * inv;
;             atomicAdd(&lcnt[ea], 1); atomicAdd(&lcnt[eb], 1);
;         }
	v_add_f32_e32 v26, v26, v100
	v_add_f32_e32 v27, v27, v101
	v_add_f32_e32 v62, v62, v102
	v_add_f32_e32 v63, v63, v103
	v_add_f32_e32 v65, v65, v104
	v_add_f32_e32 v64, v64, v105
	v_add_f32_e32 v66, v66, v106
	v_add_f32_e32 v24, v24, v107
	v_mov_b32_e32 v100, 0
	v_mov_b32_e32 v101, 0
	v_mov_b32_e32 v102, 0
	v_mov_b32_e32 v103, 0
	v_mov_b32_e32 v104, 0
	v_mov_b32_e32 v105, 0
	v_mov_b32_e32 v106, 0
	v_mov_b32_e32 v107, 0
	v_mov_b32_dpp v100, v26 row_bcast:31 row_mask:0xc bank_mask:0xf
	v_mov_b32_dpp v101, v27 row_bcast:31 row_mask:0xc bank_mask:0xf
	v_mov_b32_dpp v102, v62 row_bcast:31 row_mask:0xc bank_mask:0xf
	v_mov_b32_dpp v103, v63 row_bcast:31 row_mask:0xc bank_mask:0xf
	v_mov_b32_dpp v104, v65 row_bcast:31 row_mask:0xc bank_mask:0xf
	v_mov_b32_dpp v105, v64 row_bcast:31 row_mask:0xc bank_mask:0xf
	v_mov_b32_dpp v106, v66 row_bcast:31 row_mask:0xc bank_mask:0xf
	v_mov_b32_dpp v107, v24 row_bcast:31 row_mask:0xc bank_mask:0xf
	v_add_f32_e32 v26, v26, v100
	v_add_f32_e32 v27, v27, v101
	v_add_f32_e32 v62, v62, v102
	v_add_f32_e32 v63, v63, v103
	v_add_f32_e32 v65, v65, v104
	v_add_f32_e32 v64, v64, v105
	v_add_f32_e32 v66, v66, v106
	v_add_f32_e32 v24, v24, v107
	v_readlane_b32 s4, v26, 63
	v_readlane_b32 s5, v27, 63
	v_readlane_b32 s6, v62, 63
	v_readlane_b32 s7, v63, 63
	v_readlane_b32 s8, v65, 63
	v_readlane_b32 s9, v64, 63
	v_readlane_b32 s10, v66, 63
	v_readlane_b32 s11, v24, 63
	s_and_saveexec_b64 s[82:83], s[2:3]
	s_cbranch_execz .LBB0_2144
	s_mul_i32 s12, s49, 0xffffc020
	s_add_i32 s48, s48, s12
	v_mov_b32_e32 v62, s48
	ds_read_b128 v[24:27], v62 offset:128
	ds_read_b128 v[62:65], v62 offset:144
	s_waitcnt lgkmcnt(1)
	v_pk_add_f32 v[24:25], s[4:5], v[24:25]
	s_nop 0
	v_cmp_gt_f32_e64 s[4:5], v25, v24
	v_add_f32_e32 v26, s6, v26
	v_add_f32_e32 v27, s7, v27
	v_cndmask_b32_e64 v66, v24, v25, s[4:5]
	v_cmp_gt_f32_e64 s[6:7], v26, v66
	s_waitcnt lgkmcnt(0)
	v_add_f32_e32 v63, s9, v63
	v_add_f32_e32 v62, s8, v62
	v_cndmask_b32_e64 v66, v66, v26, s[6:7]
	v_cmp_gt_f32_e64 s[8:9], v27, v66
	v_add_f32_e32 v65, s11, v65
	v_add_f32_e32 v64, s10, v64
	v_cndmask_b32_e64 v66, v66, v27, s[8:9]
	v_cmp_gt_f32_e64 s[10:11], v62, v66
	v_cndmask_b32_e64 v67, 0, 1, s[4:5]
	s_nop 0
	v_cndmask_b32_e64 v66, v66, v62, s[10:11]
	v_cmp_gt_f32_e64 s[12:13], v63, v66
	s_nop 1
	v_cndmask_b32_e64 v66, v66, v63, s[12:13]
	v_cmp_gt_f32_e64 s[14:15], v64, v66
	s_nop 1
	v_cndmask_b32_e64 v66, v66, v64, s[14:15]
	v_cmp_ngt_f32_e64 s[16:17], v65, v66
	s_and_b64 s[22:23], s[14:15], s[16:17]
	s_and_b64 s[4:5], s[6:7], exec
	v_readfirstlane_b32 s4, v67
	s_cselect_b32 s6, 2, s4
	s_and_b64 s[4:5], s[8:9], exec
	s_cselect_b32 s6, 3, s6
	s_and_b64 s[4:5], s[10:11], exec
	s_cselect_b32 s6, 4, s6
	s_and_b64 s[4:5], s[12:13], exec
	s_cselect_b32 s6, 5, s6
	s_and_b64 s[4:5], s[14:15], exec
	s_cselect_b32 s6, 6, s6
	s_and_b64 s[4:5], s[16:17], exec
	s_cselect_b32 s46, s6, 7
	s_cmp_lg_u32 s46, 5
	s_cselect_b64 s[20:21], -1, 0
	s_cmp_lg_u32 s46, 4
	s_cselect_b64 s[14:15], -1, 0
	s_cmp_lg_u32 s46, 3
	s_cselect_b64 s[12:13], -1, 0
	s_cmp_lg_u32 s46, 2
	s_cselect_b64 s[10:11], -1, 0
	s_cmp_lg_u32 s46, 1
	s_cselect_b64 s[8:9], -1, 0
	s_cmp_eq_u32 s46, 0
	s_cselect_b64 s[6:7], -1, 0
	v_cmp_nlt_f32_e64 s[4:5], s34, v24
	s_or_b64 s[4:5], s[6:7], s[4:5]
	s_nop 0
	v_cndmask_b32_e64 v24, v24, v197, s[4:5]
	v_cmp_gt_f32_e64 s[6:7], v25, v24
	s_and_b64 s[6:7], s[8:9], s[6:7]
	s_nop 0
	v_cndmask_b32_e64 v24, v24, v25, s[6:7]
	v_cmp_gt_f32_e64 s[8:9], v26, v24
	s_and_b64 s[8:9], s[10:11], s[8:9]
	v_cndmask_b32_e64 v25, 0, -1, s[4:5]
	v_cndmask_b32_e64 v24, v24, v26, s[8:9]
	v_cndmask_b32_e32 v26, v61, v60, vcc
	v_sub_f32_e32 v22, v22, v26
	v_mul_f32_e32 v22, 0x3fb8aa3b, v22
	v_sub_f32_e32 v23, v23, v26
	v_exp_f32_e32 v22, v22
	v_mul_f32_e32 v23, 0x3fb8aa3b, v23
	v_exp_f32_e32 v23, v23
	v_cmp_gt_f32_e64 s[10:11], v27, v24
	s_and_b64 s[10:11], s[12:13], s[10:11]
	v_add_f32_e32 v22, 0, v22
	v_cndmask_b32_e64 v24, v24, v27, s[10:11]
	v_cmp_gt_f32_e64 s[12:13], v62, v24
	v_add_f32_e32 v22, v23, v22
	v_sub_f32_e32 v23, v59, v26
	s_and_b64 s[12:13], s[14:15], s[12:13]
	v_mul_f32_e32 v23, 0x3fb8aa3b, v23
	v_cndmask_b32_e64 v24, v24, v62, s[12:13]
	v_exp_f32_e32 v23, v23
	v_cmp_gt_f32_e64 s[14:15], v63, v24
	s_and_b64 s[14:15], s[20:21], s[14:15]
	v_add_f32_e32 v22, v23, v22
	v_cndmask_b32_e64 v24, v24, v63, s[14:15]
	v_cmp_ngt_f32_e64 s[20:21], v64, v24
	v_sub_f32_e32 v23, v60, v26
	s_or_b64 s[20:21], s[22:23], s[20:21]
	v_mul_f32_e32 v23, 0x3fb8aa3b, v23
	v_cndmask_b32_e64 v24, v64, v24, s[20:21]
	v_exp_f32_e32 v23, v23
	v_cmp_gt_f32_e64 s[22:23], v65, v24
	s_and_b64 s[22:23], s[16:17], s[22:23]
	s_and_b64 s[4:5], s[6:7], exec
	v_readfirstlane_b32 s4, v25
	v_add_f32_e32 v22, v23, v22
	s_cselect_b32 s6, 1, s4
	v_div_scale_f32 v23, s[4:5], v22, v22, 1.0
	v_rcp_f32_e32 v26, v23
	v_cndmask_b32_e64 v24, v24, v65, s[22:23]
	v_cndmask_b32_e64 v25, v65, v66, s[16:17]
	s_and_b64 s[4:5], s[8:9], exec
	v_fma_f32 v27, -v23, v26, 1.0
	v_fmac_f32_e32 v26, v27, v26
	v_div_scale_f32 v27, vcc, 1.0, v22, 1.0
	v_mul_f32_e32 v59, v27, v26
	v_fma_f32 v60, -v23, v59, v27
	v_fmac_f32_e32 v59, v60, v26
	v_fma_f32 v23, -v23, v59, v27
	v_div_fmas_f32 v23, v23, v26, v59
	v_div_fixup_f32 v26, v23, v22, 1.0
	v_sub_f32_e32 v22, v24, v25
	v_mul_f32_e32 v22, 0x3fb8aa3b, v22
	v_exp_f32_e32 v24, v22
	s_cselect_b32 s6, 2, s6
	s_and_b64 s[4:5], s[10:11], exec
	s_cselect_b32 s6, 3, s6
	v_add_f32_e32 v22, 1.0, v24
	v_div_scale_f32 v23, s[4:5], v22, v22, 1.0
	v_rcp_f32_e32 v25, v23
	s_and_b64 s[4:5], s[12:13], exec
	s_cselect_b32 s6, 4, s6
	s_and_b64 s[4:5], s[14:15], exec
	s_cselect_b32 s6, 5, s6
	s_and_b64 s[4:5], s[20:21], exec
	v_fma_f32 v27, -v23, v25, 1.0
	s_cselect_b32 s6, s6, 6
	s_and_b64 s[4:5], s[22:23], exec
	v_fmac_f32_e32 v25, v27, v25
	v_div_scale_f32 v27, vcc, 1.0, v22, 1.0
	s_cselect_b32 s8, 7, s6
	v_mul_f32_e32 v59, v27, v25
	s_lshl_b32 s4, s49, 3
	s_ashr_i32 s81, s80, 31
	v_fma_f32 v60, -v23, v59, v27
	s_or_b32 s9, s46, s4
	s_add_i32 s12, s8, s4
	s_lshl_b64 s[4:5], s[80:81], 2
	v_fmac_f32_e32 v59, v60, v25
	s_add_u32 s6, s52, s4
	v_fma_f32 v23, -v23, v59, v27
	s_addc_u32 s7, s53, s5
	s_add_i32 s10, s80, 1
	v_div_fmas_f32 v23, v23, v25, v59
	s_ashr_i32 s11, s10, 31
	v_div_fixup_f32 v25, v23, v22, 1.0
	v_mov_b32_e32 v22, s9
	v_mov_b32_e32 v23, s12
	s_add_u32 s4, s40, s4
	global_store_dwordx2 v129, v[22:23], s[6:7]
	global_store_dword v129, v2, s[78:79]
	v_mul_f32_e32 v2, v26, v25
	s_addc_u32 s5, s41, s5
	global_store_dword v129, v2, s[4:5]
	s_lshl_b64 s[4:5], s[10:11], 2
	v_mul_f32_e32 v2, v26, v24
	s_add_u32 s4, s40, s4
	v_mul_f32_e32 v2, v2, v25
	s_addc_u32 s5, s41, s5
	global_store_dword v129, v2, s[4:5]
	s_mov_b64 s[4:5], exec
	v_mbcnt_lo_u32_b32 v2, s4, 0
	v_mbcnt_hi_u32_b32 v2, s5, v2
	v_cmp_eq_u32_e32 vcc, 0, v2
	s_and_saveexec_b64 s[6:7], vcc
	s_cbranch_execz .LBB0_2148
	s_lshl_b32 s9, s9, 2
	s_add_i32 s9, s9, 0
	s_bcnt1_i32_b64 s4, s[4:5]
	v_mov_b32_e32 v2, s9
	v_mov_b32_e32 v22, s4
	ds_add_u32 v2, v22

;     __device__ __forceinline__ const char* aptr(const Unit& u) const { return (const char*)(A + (size_t)u.pm * BM * lda); }
; template <class Epi, class Sched>
; __device__ __forceinline__ void gemm_phase(const int WID_, PG8_LAS unsigned char* lds, const Sched& S, const Epi& E) {
;     ...
;         const char* nA = has_next ? S.aptr(nxt) : cA; const char* nB = has_next ? S.bptr(nxt) : cB;
;         if (has_next) PG8_GOFF(vgn, nxt); else { if constexpr (GA) { _Pragma("unroll") for (int h_ = 0; h_ < 2; ++h_) _Pragma("unroll") for (int i_ = 0; i_ < 2; ++i_) vgn[h_][i_] = vgc[h_][i_]; } }
;         for (int t = 0; t < nt; t += 2) {
;             const bool last = (t == nt - 2);
;             const char* a1 = cA + (size_t)(t + 1) * kstep;
;             const char* a2 = last ? nA : cA + (size_t)(t + 2) * kstep; const char* b2 = last ? nB : cB + (size_t)(t + 2) * kstep;
;             const char* a3 = a2 + kstep; const char* b3 = b2 + kstep;
;             PG8_LDB(B0, 0, 0); PG8_LDB(B1, 0, 1); PG8_SCHED; PG8_LDA(At, 0, 0); PG8_STAGE_A(PG8_SA(1, 1), a1 + hstepA, 1, false);
;             PG8_WAIT_V(8); PG8_WAIT_L(0); PG8_BAR; PG8_MMA(0, 0, At, B0); PG8_MMA(0, 1, At, B1); PG8_BAR; PG8_SCHED;
;             PG8_LDA(At, 0, 1); PG8_STAGE(PG8_SB(0, 0), b2, voffB); PG8_STAGE(PG8_SB(0, 1), b2 + hstepB, voffB); PG8_STAGE_A(PG8_SA(0, 0), a2, 0, last);
;             PG8_WAIT_V(8); PG8_WAIT_L(0); PG8_BAR; PG8_MMA(1, 0, At, B0); PG8_MMA(1, 1, At, B1); PG8_BAR; PG8_SCHED;
;             PG8_LDB(B0, 1, 0); PG8_LDB(B1, 1, 1); PG8_SCHED; PG8_LDA(At, 1, 0); PG8_STAGE_A(PG8_SA(0, 1), a2 + hstepA, 1, last);
;             PG8_WAIT_V(8); PG8_WAIT_L(0); PG8_BAR; PG8_MMA(0, 0, At, B0); PG8_MMA(0, 1, At, B1); PG8_BAR; PG8_SCHED;
;             PG8_LDA(At, 1, 1); PG8_STAGE(PG8_SB(1, 0), b3, voffB); PG8_STAGE(PG8_SB(1, 1), b3 + hstepB, voffB); PG8_STAGE_A(PG8_SA(1, 0), a3, 0, last);
;             PG8_WAIT_V(8); PG8_WAIT_L(0); PG8_BAR; PG8_MMA(1, 0, At, B0); PG8_MMA(1, 1, At, B1); PG8_BAR; PG8_SCHED;
;         }
;         if (wr == 0) PG8_BAR;
;         E(acc, cur, wr, wc, fr, fq);
;         if (!has_next) break;
; #pragma unroll
;         for (int a = 0; a < 2; ++a)
; #pragma unroll
;             for (int b = 0; b < 2; ++b)
; #pragma unroll
;                 for (int m = 0; m < 4; ++m)
; #pragma unroll
;                     for (int n = 0; n < 2; ++n) acc[a][b][m][n] = (f32x4){0.f, 0.f, 0.f, 0.f};
.LBB0_2293:
	v_mov_b32_e32 v139, v133
	v_mov_b32_e32 v141, v133
	v_mov_b32_e32 v0, 0
	v_lshl_add_u64 v[142:143], s[92:93], 0, v[138:139]
	v_lshl_add_u64 v[144:145], s[92:93], 0, v[140:141]
	s_mov_b32 s11, -2
	s_mov_b64 s[4:5], 0x100
	v_mov_b32_e32 v1, v0
	v_pk_mov_b32 v[2:3], v[0:1], v[0:1]
	v_pk_mov_b32 v[4:5], v[0:1], v[0:1]
	v_pk_mov_b32 v[6:7], v[0:1], v[0:1]
	v_pk_mov_b32 v[8:9], v[0:1], v[0:1]
	v_pk_mov_b32 v[10:11], v[0:1], v[0:1]
	v_pk_mov_b32 v[12:13], v[0:1], v[0:1]
	v_pk_mov_b32 v[14:15], v[0:1], v[0:1]
	v_pk_mov_b32 v[16:17], v[0:1], v[0:1]
	v_pk_mov_b32 v[18:19], v[0:1], v[0:1]
	v_pk_mov_b32 v[20:21], v[0:1], v[0:1]
	v_pk_mov_b32 v[22:23], v[0:1], v[0:1]
	v_pk_mov_b32 v[24:25], v[0:1], v[0:1]
	v_pk_mov_b32 v[26:27], v[0:1], v[0:1]
	v_pk_mov_b32 v[28:29], v[0:1], v[0:1]
	v_pk_mov_b32 v[30:31], v[0:1], v[0:1]
	v_pk_mov_b32 v[32:33], v[0:1], v[0:1]
	v_pk_mov_b32 v[34:35], v[0:1], v[0:1]
	v_pk_mov_b32 v[36:37], v[0:1], v[0:1]
	v_pk_mov_b32 v[38:39], v[0:1], v[0:1]
	v_pk_mov_b32 v[40:41], v[0:1], v[0:1]
	v_pk_mov_b32 v[42:43], v[0:1], v[0:1]
	v_pk_mov_b32 v[44:45], v[0:1], v[0:1]
	v_pk_mov_b32 v[46:47], v[0:1], v[0:1]
	v_pk_mov_b32 v[48:49], v[0:1], v[0:1]
	v_pk_mov_b32 v[50:51], v[0:1], v[0:1]
	v_pk_mov_b32 v[52:53], v[0:1], v[0:1]
	v_pk_mov_b32 v[54:55], v[0:1], v[0:1]
	v_pk_mov_b32 v[56:57], v[0:1], v[0:1]
	v_pk_mov_b32 v[58:59], v[0:1], v[0:1]
	v_pk_mov_b32 v[60:61], v[0:1], v[0:1]
	v_pk_mov_b32 v[62:63], v[0:1], v[0:1]
	v_pk_mov_b32 v[64:65], v[0:1], v[0:1]
	v_pk_mov_b32 v[66:67], v[0:1], v[0:1]
	v_pk_mov_b32 v[68:69], v[0:1], v[0:1]
	v_pk_mov_b32 v[70:71], v[0:1], v[0:1]
	v_pk_mov_b32 v[72:73], v[0:1], v[0:1]
	v_pk_mov_b32 v[74:75], v[0:1], v[0:1]
	v_pk_mov_b32 v[76:77], v[0:1], v[0:1]
	v_pk_mov_b32 v[78:79], v[0:1], v[0:1]
	v_pk_mov_b32 v[80:81], v[0:1], v[0:1]
	v_pk_mov_b32 v[82:83], v[0:1], v[0:1]
	v_pk_mov_b32 v[84:85], v[0:1], v[0:1]
	v_pk_mov_b32 v[86:87], v[0:1], v[0:1]
	v_pk_mov_b32 v[88:89], v[0:1], v[0:1]
	v_pk_mov_b32 v[90:91], v[0:1], v[0:1]
	v_pk_mov_b32 v[92:93], v[0:1], v[0:1]
	v_pk_mov_b32 v[94:95], v[0:1], v[0:1]
	v_pk_mov_b32 v[96:97], v[0:1], v[0:1]
	v_pk_mov_b32 v[98:99], v[0:1], v[0:1]
	v_pk_mov_b32 v[100:101], v[0:1], v[0:1]
	v_pk_mov_b32 v[102:103], v[0:1], v[0:1]
	v_pk_mov_b32 v[104:105], v[0:1], v[0:1]
	v_pk_mov_b32 v[106:107], v[0:1], v[0:1]
	v_pk_mov_b32 v[108:109], v[0:1], v[0:1]
	v_pk_mov_b32 v[110:111], v[0:1], v[0:1]
	v_pk_mov_b32 v[112:113], v[0:1], v[0:1]
	v_pk_mov_b32 v[114:115], v[0:1], v[0:1]
	v_pk_mov_b32 v[116:117], v[0:1], v[0:1]
	v_pk_mov_b32 v[118:119], v[0:1], v[0:1]
	v_pk_mov_b32 v[120:121], v[0:1], v[0:1]
	v_pk_mov_b32 v[122:123], v[0:1], v[0:1]
	v_pk_mov_b32 v[124:125], v[0:1], v[0:1]
	v_pk_mov_b32 v[126:127], v[0:1], v[0:1]

; #define PG8_WAIT_V(n) asm volatile("s_waitcnt vmcnt(" #n ")" ::: "memory")
; template <class Epi, class Sched>
; __device__ __forceinline__ void gemm_phase(const int WID_, PG8_LAS unsigned char* lds, const Sched& S, const Epi& E) {
;     ...
;         const bool has_next = S.next(ui + 1, nxt);
;         const char* nA = has_next ? S.aptr(nxt) : cA; const char* nB = has_next ? S.bptr(nxt) : cB;
;         if (has_next) PG8_GOFF(vgn, nxt); else { if constexpr (GA) { _Pragma("unroll") for (int h_ = 0; h_ < 2; ++h_) _Pragma("unroll") for (int i_ = 0; i_ < 2; ++i_) vgn[h_][i_] = vgc[h_][i_]; } }
;         for (int t = 0; t < nt; t += 2) {
;             const bool last = (t == nt - 2);
;             const char* a1 = cA + (size_t)(t + 1) * kstep;
;             const char* a2 = last ? nA : cA + (size_t)(t + 2) * kstep; const char* b2 = last ? nB : cB + (size_t)(t + 2) * kstep;
;             const char* a3 = a2 + kstep; const char* b3 = b2 + kstep;
;             PG8_LDB(B0, 0, 0); PG8_LDB(B1, 0, 1); PG8_SCHED; PG8_LDA(At, 0, 0); PG8_STAGE_A(PG8_SA(1, 1), a1 + hstepA, 1, false);
;             PG8_WAIT_V(8); PG8_WAIT_L(0); PG8_BAR; PG8_MMA(0, 0, At, B0); PG8_MMA(0, 1, At, B1); PG8_BAR; PG8_SCHED;
;             PG8_LDA(At, 0, 1); PG8_STAGE(PG8_SB(0, 0), b2, voffB); PG8_STAGE(PG8_SB(0, 1), b2 + hstepB, voffB); PG8_STAGE_A(PG8_SA(0, 0), a2, 0, last);
;             PG8_WAIT_V(8); PG8_WAIT_L(0); PG8_BAR; PG8_MMA(1, 0, At, B0); PG8_MMA(1, 1, At, B1); PG8_BAR; PG8_SCHED;
;             PG8_LDB(B0, 1, 0); PG8_LDB(B1, 1, 1); PG8_SCHED; PG8_LDA(At, 1, 0); PG8_STAGE_A(PG8_SA(0, 1), a2 + hstepA, 1, last);
;             PG8_WAIT_V(8); PG8_WAIT_L(0); PG8_BAR; PG8_MMA(0, 0, At, B0); PG8_MMA(0, 1, At, B1); PG8_BAR; PG8_SCHED;
;             PG8_LDA(At, 1, 1); PG8_STAGE(PG8_SB(1, 0), b3, voffB); PG8_STAGE(PG8_SB(1, 1), b3 + hstepB, voffB); PG8_STAGE_A(PG8_SA(1, 0), a3, 0, last);
;             PG8_WAIT_V(8); PG8_WAIT_L(0); PG8_BAR; PG8_MMA(1, 0, At, B0); PG8_MMA(1, 1, At, B1); PG8_BAR; PG8_SCHED;
;         }
;         if (wr == 0) PG8_BAR;
;         E(acc, cur, wr, wc, fr, fq);
;         if (!has_next) break;
; #pragma unroll
;         for (int a = 0; a < 2; ++a)
; #pragma unroll
;             for (int b = 0; b < 2; ++b)
; #pragma unroll
;                 for (int m = 0; m < 4; ++m)
; #pragma unroll
;                     for (int n = 0; n < 2; ++n) acc[a][b][m][n] = (f32x4){0.f, 0.f, 0.f, 0.f};
.LBB0_2361:
	s_lshl_b64 s[36:37], s[30:31], 18
	s_add_u32 s36, s18, s36
	s_addc_u32 s37, s19, s37
	s_and_b64 s[42:43], s[0:1], exec
	s_cselect_b32 s31, s37, s39
	s_cselect_b32 s59, s36, s38
	s_add_u32 s38, s38, 0x20080
	s_addc_u32 s39, s39, 0
	s_add_u32 s60, s40, 0x100
	v_mov_b32_e32 v0, 0
	s_addc_u32 s61, s41, 0
	s_mov_b32 s62, -2
	v_mov_b32_e32 v1, v0
	v_pk_mov_b32 v[2:3], v[0:1], v[0:1]
	v_pk_mov_b32 v[4:5], v[0:1], v[0:1]
	v_pk_mov_b32 v[6:7], v[0:1], v[0:1]
	v_pk_mov_b32 v[8:9], v[0:1], v[0:1]
	v_pk_mov_b32 v[10:11], v[0:1], v[0:1]
	v_pk_mov_b32 v[12:13], v[0:1], v[0:1]
	v_pk_mov_b32 v[14:15], v[0:1], v[0:1]
	v_pk_mov_b32 v[16:17], v[0:1], v[0:1]
	v_pk_mov_b32 v[18:19], v[0:1], v[0:1]
	v_pk_mov_b32 v[20:21], v[0:1], v[0:1]
	v_pk_mov_b32 v[22:23], v[0:1], v[0:1]
	v_pk_mov_b32 v[24:25], v[0:1], v[0:1]
	v_pk_mov_b32 v[26:27], v[0:1], v[0:1]
	v_pk_mov_b32 v[28:29], v[0:1], v[0:1]
	v_pk_mov_b32 v[30:31], v[0:1], v[0:1]
	v_pk_mov_b32 v[32:33], v[0:1], v[0:1]
	v_pk_mov_b32 v[34:35], v[0:1], v[0:1]
	v_pk_mov_b32 v[36:37], v[0:1], v[0:1]
	v_pk_mov_b32 v[38:39], v[0:1], v[0:1]
	v_pk_mov_b32 v[40:41], v[0:1], v[0:1]
	v_pk_mov_b32 v[42:43], v[0:1], v[0:1]
	v_pk_mov_b32 v[44:45], v[0:1], v[0:1]
	v_pk_mov_b32 v[46:47], v[0:1], v[0:1]
	v_pk_mov_b32 v[48:49], v[0:1], v[0:1]
	v_pk_mov_b32 v[50:51], v[0:1], v[0:1]
	v_pk_mov_b32 v[52:53], v[0:1], v[0:1]
	v_pk_mov_b32 v[54:55], v[0:1], v[0:1]
	v_pk_mov_b32 v[56:57], v[0:1], v[0:1]
	v_pk_mov_b32 v[58:59], v[0:1], v[0:1]
	v_pk_mov_b32 v[60:61], v[0:1], v[0:1]
	v_pk_mov_b32 v[62:63], v[0:1], v[0:1]
	v_pk_mov_b32 v[64:65], v[0:1], v[0:1]
	v_pk_mov_b32 v[66:67], v[0:1], v[0:1]
	v_pk_mov_b32 v[68:69], v[0:1], v[0:1]
	v_pk_mov_b32 v[70:71], v[0:1], v[0:1]
	v_pk_mov_b32 v[72:73], v[0:1], v[0:1]
	v_pk_mov_b32 v[74:75], v[0:1], v[0:1]
	v_pk_mov_b32 v[76:77], v[0:1], v[0:1]
	v_pk_mov_b32 v[78:79], v[0:1], v[0:1]
	v_pk_mov_b32 v[80:81], v[0:1], v[0:1]
	v_pk_mov_b32 v[82:83], v[0:1], v[0:1]
	v_pk_mov_b32 v[84:85], v[0:1], v[0:1]
	v_pk_mov_b32 v[86:87], v[0:1], v[0:1]
	v_pk_mov_b32 v[88:89], v[0:1], v[0:1]
	v_pk_mov_b32 v[90:91], v[0:1], v[0:1]
	v_pk_mov_b32 v[92:93], v[0:1], v[0:1]
	v_pk_mov_b32 v[94:95], v[0:1], v[0:1]
	v_pk_mov_b32 v[96:97], v[0:1], v[0:1]
	v_pk_mov_b32 v[98:99], v[0:1], v[0:1]
	v_pk_mov_b32 v[100:101], v[0:1], v[0:1]
	v_pk_mov_b32 v[102:103], v[0:1], v[0:1]
	v_pk_mov_b32 v[104:105], v[0:1], v[0:1]
	v_pk_mov_b32 v[106:107], v[0:1], v[0:1]
	v_pk_mov_b32 v[108:109], v[0:1], v[0:1]
	v_pk_mov_b32 v[110:111], v[0:1], v[0:1]
	v_pk_mov_b32 v[112:113], v[0:1], v[0:1]
	v_pk_mov_b32 v[114:115], v[0:1], v[0:1]
	v_pk_mov_b32 v[116:117], v[0:1], v[0:1]
	v_pk_mov_b32 v[118:119], v[0:1], v[0:1]
	v_pk_mov_b32 v[120:121], v[0:1], v[0:1]
	v_pk_mov_b32 v[122:123], v[0:1], v[0:1]
	v_pk_mov_b32 v[124:125], v[0:1], v[0:1]
	v_pk_mov_b32 v[126:127], v[0:1], v[0:1]
